# speedup vs baseline: 1.0405x; 1.0405x over previous
.LBB1_4:
	s_or_b64 exec, exec, s[2:3]
	s_load_dwordx2 s[12:13], s[0:1], 0x0
	s_mov_b64 s[0:1], src_shared_base
	s_cmp_lg_u32 0, -1
	s_cselect_b32 s0, s1, 0
	s_cselect_b32 s1, 0, 0
	v_mov_b32_e32 v2, s1
	v_mov_b32_e32 v3, s0
	s_waitcnt lgkmcnt(0)
	s_barrier
	flat_load_dword v2, v[2:3] sc0 sc1
	s_waitcnt vmcnt(0)
	s_movk_i32 s2, 0xff
	v_cmp_lt_u32_e32 vcc, s2, v0
	v_lshlrev_b32_e32 v130, 4, v0
	v_lshrrev_b32_e32 v3, 1, v0
	v_bfe_u32 v202, v0, 5, 1
	v_and_b32_e32 v1, 3, v0
	v_and_b32_e32 v4, 64, v130
	v_and_b32_e32 v3, 12, v3
	v_and_b32_e32 v5, 0x1df0, v130
	v_mul_u32_u24_e32 v6, 0x820, v202
	v_or3_b32 v1, v1, v4, v3
	v_lshl_or_b32 v3, v202, 13, v5
	v_lshl_add_u32 v195, v1, 4, v6
	s_mov_b32 s1, 0
	s_movk_i32 s0, 0x820
	v_add_u32_e32 v1, 0, v195
	v_add_u32_e32 v194, 0, v3
	s_waitcnt lgkmcnt(0)
	s_barrier
	v_readfirstlane_b32 s14, v2
	s_ashr_i32 s2, s14, 1
	s_and_b32 s3, s14, 4
	s_and_b32 s2, s2, -8
	s_lshl_b32 s6, s14, 5
	s_or_b32 s2, s2, s3
	s_and_b32 s28, s6, 0x60
	s_ashr_i32 s33, s2, 2
	s_add_i32 s2, s33, s28
	s_ashr_i32 s3, s2, 31
	s_lshl_b64 s[20:21], s[2:3], 7
	s_bfe_u32 s29, s14, 0x10003
	v_lshrrev_b32_e32 v1, 6, v0
	v_and_b32_e32 v240, 31, v0
	v_bfe_u32 v241, v0, 5, 1
	v_readfirstlane_b32 s34, v1
	s_lshl_b32 s35, s20, 12
	s_add_u32 s40, s12, s35
	s_addc_u32 s41, s13, 0
	s_add_u32 s42, s40, 0x10000
	s_addc_u32 s43, s41, 0
	s_add_u32 s44, s42, 0x10000
	s_addc_u32 s45, s43, 0
	s_add_u32 s46, s44, 0x10000
	s_addc_u32 s47, s45, 0
	s_add_u32 s48, s46, 0x10000
	s_addc_u32 s49, s47, 0
	s_add_u32 s50, s48, 0x10000
	s_addc_u32 s51, s49, 0
	s_add_u32 s52, s50, 0x10000
	s_addc_u32 s53, s51, 0
	s_add_u32 s54, s52, 0x10000
	s_addc_u32 s55, s53, 0
	s_lshl_b32 s35, s29, 20
	s_add_u32 s56, s10, s35
	s_addc_u32 s57, s11, 0
	s_lshl_b32 s35, s34, 10
	v_lshlrev_b32_e32 v1, 4, v240
	v_lshl_add_u32 v1, v241, 13, v1
	v_add_u32_e32 v239, s35, v1
	v_bfe_u32 v1, v240, 2, 1
	v_and_b32_e32 v242, 3, v240
	v_lshrrev_b32_e32 v243, 3, v240
	v_lshl_add_u32 v242, v243, 2, v242
	v_lshl_add_u32 v1, v1, 6, v242
	v_mul_u32_u24_e32 v1, 0x110, v1
	v_lshl_add_u32 v236, v241, 4, v1
	v_lshrrev_b32_e32 v1, 5, v0
	v_lshlrev_b32_e32 v242, 12, v1
	v_lshl_add_u32 v238, v240, 4, v242
	v_mul_u32_u24_e32 v242, 0x110, v1
	v_lshl_add_u32 v237, v240, 3, v242
	global_load_dwordx4 v[204:207], v238, s[40:41]
	global_load_dwordx4 v[208:211], v238, s[42:43]
	global_load_dwordx4 v[212:215], v238, s[44:45]
	global_load_dwordx4 v[216:219], v238, s[46:47]
	global_load_dwordx4 v[220:223], v238, s[48:49]
	global_load_dwordx4 v[224:227], v238, s[50:51]
	global_load_dwordx4 v[228:231], v238, s[52:53]
	global_load_dwordx4 v[232:235], v238, s[54:55]
	global_load_dwordx4 v[146:149], v239, s[56:57]
	global_load_dwordx4 v[150:153], v239, s[56:57] offset:512
	s_add_u32 s56, s56, 0x4000
	s_addc_u32 s57, s57, 0
	global_load_dwordx4 v[154:157], v239, s[56:57]
	global_load_dwordx4 v[158:161], v239, s[56:57] offset:512
	s_add_u32 s56, s56, 0x4000
	s_addc_u32 s57, s57, 0
	global_load_dwordx4 v[162:165], v239, s[56:57]
	global_load_dwordx4 v[166:169], v239, s[56:57] offset:512
	s_add_u32 s56, s56, 0x4000
	s_addc_u32 s57, s57, 0
	global_load_dwordx4 v[170:173], v239, s[56:57]
	global_load_dwordx4 v[174:177], v239, s[56:57] offset:512
	s_add_u32 s56, s56, 0x4000
	s_addc_u32 s57, s57, 0
	global_load_dwordx4 v[178:181], v239, s[56:57]
	global_load_dwordx4 v[182:185], v239, s[56:57] offset:512
	s_add_u32 s56, s56, 0x4000
	s_addc_u32 s57, s57, 0
	global_load_dwordx4 v[186:189], v239, s[56:57]
	global_load_dwordx4 v[190:193], v239, s[56:57] offset:512
	s_add_u32 s56, s56, 0x4000
	s_addc_u32 s57, s57, 0
	global_load_dwordx4 v[194:197], v239, s[56:57]
	global_load_dwordx4 v[198:201], v239, s[56:57] offset:512
	s_add_u32 s56, s56, 0x4000
	s_addc_u32 s57, s57, 0
	s_waitcnt vmcnt(21)
	v_cvt_pk_f16_f32 v204, v204, v205
	v_cvt_pk_f16_f32 v205, v206, v207
	ds_write_b64 v237, v[204:205]
	s_waitcnt vmcnt(20)
	v_cvt_pk_f16_f32 v208, v208, v209
	v_cvt_pk_f16_f32 v209, v210, v211
	ds_write_b64 v237, v[208:209] offset:4352
	s_waitcnt vmcnt(19)
	v_cvt_pk_f16_f32 v212, v212, v213
	v_cvt_pk_f16_f32 v213, v214, v215
	ds_write_b64 v237, v[212:213] offset:8704
	s_waitcnt vmcnt(18)
	v_cvt_pk_f16_f32 v216, v216, v217
	v_cvt_pk_f16_f32 v217, v218, v219
	ds_write_b64 v237, v[216:217] offset:13056
	s_waitcnt vmcnt(17)
	v_cvt_pk_f16_f32 v220, v220, v221
	v_cvt_pk_f16_f32 v221, v222, v223
	ds_write_b64 v237, v[220:221] offset:17408
	s_waitcnt vmcnt(16)
	v_cvt_pk_f16_f32 v224, v224, v225
	v_cvt_pk_f16_f32 v225, v226, v227
	ds_write_b64 v237, v[224:225] offset:21760
	s_waitcnt vmcnt(15)
	v_cvt_pk_f16_f32 v228, v228, v229
	v_cvt_pk_f16_f32 v229, v230, v231
	ds_write_b64 v237, v[228:229] offset:26112
	s_waitcnt vmcnt(14)
	v_cvt_pk_f16_f32 v232, v232, v233
	v_cvt_pk_f16_f32 v233, v234, v235
	ds_write_b64 v237, v[232:233] offset:30464
	global_load_dwordx4 v[204:207], v238, s[40:41] offset:512
	global_load_dwordx4 v[208:211], v238, s[42:43] offset:512
	global_load_dwordx4 v[212:215], v238, s[44:45] offset:512
	global_load_dwordx4 v[216:219], v238, s[46:47] offset:512
	global_load_dwordx4 v[220:223], v238, s[48:49] offset:512
	global_load_dwordx4 v[224:227], v238, s[50:51] offset:512
	global_load_dwordx4 v[228:231], v238, s[52:53] offset:512
	global_load_dwordx4 v[232:235], v238, s[54:55] offset:512
	s_waitcnt lgkmcnt(0)
	s_barrier
	ds_read_b128 v[130:133], v236
	ds_read_b128 v[134:137], v236 offset:4352
	ds_read_b128 v[138:141], v236 offset:8704
	ds_read_b128 v[142:145], v236 offset:13056
	s_waitcnt vmcnt(20)
	s_waitcnt lgkmcnt(3)
	v_mfma_f32_32x32x16_f16 v[82:97], v[130:133], v[146:149], 0
	v_mfma_f32_32x32x16_f16 v[50:65], v[130:133], v[150:153], 0
	ds_read_b128 v[130:133], v236 offset:32
	s_waitcnt lgkmcnt(3)
	v_mfma_f32_32x32x16_f16 v[114:129], v[134:137], v[146:149], 0
	v_mfma_f32_32x32x16_f16 v[34:49], v[134:137], v[150:153], 0
	ds_read_b128 v[134:137], v236 offset:4384
	s_waitcnt lgkmcnt(3)
	v_mfma_f32_32x32x16_f16 v[98:113], v[138:141], v[146:149], 0
	v_mfma_f32_32x32x16_f16 v[18:33], v[138:141], v[150:153], 0
	ds_read_b128 v[138:141], v236 offset:8736
	s_waitcnt lgkmcnt(3)
	v_mfma_f32_32x32x16_f16 v[66:81], v[142:145], v[146:149], 0
	v_mfma_f32_32x32x16_f16 v[2:17], v[142:145], v[150:153], 0
	ds_read_b128 v[142:145], v236 offset:13088
	global_load_dwordx4 v[146:149], v239, s[56:57]
	global_load_dwordx4 v[150:153], v239, s[56:57] offset:512
	s_add_u32 s56, s56, 0x4000
	s_addc_u32 s57, s57, 0
	s_waitcnt vmcnt(20)
	s_waitcnt lgkmcnt(3)
	v_mfma_f32_32x32x16_f16 v[82:97], v[130:133], v[154:157], v[82:97]
	v_mfma_f32_32x32x16_f16 v[50:65], v[130:133], v[158:161], v[50:65]
	ds_read_b128 v[130:133], v236 offset:64
	s_waitcnt lgkmcnt(3)
	v_mfma_f32_32x32x16_f16 v[114:129], v[134:137], v[154:157], v[114:129]
	v_mfma_f32_32x32x16_f16 v[34:49], v[134:137], v[158:161], v[34:49]
	ds_read_b128 v[134:137], v236 offset:4416
	s_waitcnt lgkmcnt(3)
	v_mfma_f32_32x32x16_f16 v[98:113], v[138:141], v[154:157], v[98:113]
	v_mfma_f32_32x32x16_f16 v[18:33], v[138:141], v[158:161], v[18:33]
	ds_read_b128 v[138:141], v236 offset:8768
	s_waitcnt lgkmcnt(3)
	v_mfma_f32_32x32x16_f16 v[66:81], v[142:145], v[154:157], v[66:81]
	v_mfma_f32_32x32x16_f16 v[2:17], v[142:145], v[158:161], v[2:17]
	ds_read_b128 v[142:145], v236 offset:13120
	global_load_dwordx4 v[154:157], v239, s[56:57]
	global_load_dwordx4 v[158:161], v239, s[56:57] offset:512
	s_add_u32 s56, s56, 0x4000
	s_addc_u32 s57, s57, 0
	s_waitcnt vmcnt(20)
	s_waitcnt lgkmcnt(3)
	v_mfma_f32_32x32x16_f16 v[82:97], v[130:133], v[162:165], v[82:97]
	v_mfma_f32_32x32x16_f16 v[50:65], v[130:133], v[166:169], v[50:65]
	ds_read_b128 v[130:133], v236 offset:96
	s_waitcnt lgkmcnt(3)
	v_mfma_f32_32x32x16_f16 v[114:129], v[134:137], v[162:165], v[114:129]
	v_mfma_f32_32x32x16_f16 v[34:49], v[134:137], v[166:169], v[34:49]
	ds_read_b128 v[134:137], v236 offset:4448
	s_waitcnt lgkmcnt(3)
	v_mfma_f32_32x32x16_f16 v[98:113], v[138:141], v[162:165], v[98:113]
	v_mfma_f32_32x32x16_f16 v[18:33], v[138:141], v[166:169], v[18:33]
	ds_read_b128 v[138:141], v236 offset:8800
	s_waitcnt lgkmcnt(3)
	v_mfma_f32_32x32x16_f16 v[66:81], v[142:145], v[162:165], v[66:81]
	v_mfma_f32_32x32x16_f16 v[2:17], v[142:145], v[166:169], v[2:17]
	ds_read_b128 v[142:145], v236 offset:13152
	global_load_dwordx4 v[162:165], v239, s[56:57]
	global_load_dwordx4 v[166:169], v239, s[56:57] offset:512
	s_add_u32 s56, s56, 0x4000
	s_addc_u32 s57, s57, 0
	s_waitcnt vmcnt(20)
	s_waitcnt lgkmcnt(3)
	v_mfma_f32_32x32x16_f16 v[82:97], v[130:133], v[170:173], v[82:97]
	v_mfma_f32_32x32x16_f16 v[50:65], v[130:133], v[174:177], v[50:65]
	ds_read_b128 v[130:133], v236 offset:128
	s_waitcnt lgkmcnt(3)
	v_mfma_f32_32x32x16_f16 v[114:129], v[134:137], v[170:173], v[114:129]
	v_mfma_f32_32x32x16_f16 v[34:49], v[134:137], v[174:177], v[34:49]
	ds_read_b128 v[134:137], v236 offset:4480
	s_waitcnt lgkmcnt(3)
	v_mfma_f32_32x32x16_f16 v[98:113], v[138:141], v[170:173], v[98:113]
	v_mfma_f32_32x32x16_f16 v[18:33], v[138:141], v[174:177], v[18:33]
	ds_read_b128 v[138:141], v236 offset:8832
	s_waitcnt lgkmcnt(3)
	v_mfma_f32_32x32x16_f16 v[66:81], v[142:145], v[170:173], v[66:81]
	v_mfma_f32_32x32x16_f16 v[2:17], v[142:145], v[174:177], v[2:17]
	ds_read_b128 v[142:145], v236 offset:13184
	global_load_dwordx4 v[170:173], v239, s[56:57]
	global_load_dwordx4 v[174:177], v239, s[56:57] offset:512
	s_add_u32 s56, s56, 0x4000
	s_addc_u32 s57, s57, 0
	s_waitcnt vmcnt(20)
	s_waitcnt lgkmcnt(3)
	v_mfma_f32_32x32x16_f16 v[82:97], v[130:133], v[178:181], v[82:97]
	v_mfma_f32_32x32x16_f16 v[50:65], v[130:133], v[182:185], v[50:65]
	ds_read_b128 v[130:133], v236 offset:160
	s_waitcnt lgkmcnt(3)
	v_mfma_f32_32x32x16_f16 v[114:129], v[134:137], v[178:181], v[114:129]
	v_mfma_f32_32x32x16_f16 v[34:49], v[134:137], v[182:185], v[34:49]
	ds_read_b128 v[134:137], v236 offset:4512
	s_waitcnt lgkmcnt(3)
	v_mfma_f32_32x32x16_f16 v[98:113], v[138:141], v[178:181], v[98:113]
	v_mfma_f32_32x32x16_f16 v[18:33], v[138:141], v[182:185], v[18:33]
	ds_read_b128 v[138:141], v236 offset:8864
	s_waitcnt lgkmcnt(3)
	v_mfma_f32_32x32x16_f16 v[66:81], v[142:145], v[178:181], v[66:81]
	v_mfma_f32_32x32x16_f16 v[2:17], v[142:145], v[182:185], v[2:17]
	ds_read_b128 v[142:145], v236 offset:13216
	global_load_dwordx4 v[178:181], v239, s[56:57]
	global_load_dwordx4 v[182:185], v239, s[56:57] offset:512
	s_add_u32 s56, s56, 0x4000
	s_addc_u32 s57, s57, 0
	s_waitcnt vmcnt(20)
	s_waitcnt lgkmcnt(3)
	v_mfma_f32_32x32x16_f16 v[82:97], v[130:133], v[186:189], v[82:97]
	v_mfma_f32_32x32x16_f16 v[50:65], v[130:133], v[190:193], v[50:65]
	ds_read_b128 v[130:133], v236 offset:192
	s_waitcnt lgkmcnt(3)
	v_mfma_f32_32x32x16_f16 v[114:129], v[134:137], v[186:189], v[114:129]
	v_mfma_f32_32x32x16_f16 v[34:49], v[134:137], v[190:193], v[34:49]
	ds_read_b128 v[134:137], v236 offset:4544
	s_waitcnt lgkmcnt(3)
	v_mfma_f32_32x32x16_f16 v[98:113], v[138:141], v[186:189], v[98:113]
	v_mfma_f32_32x32x16_f16 v[18:33], v[138:141], v[190:193], v[18:33]
	ds_read_b128 v[138:141], v236 offset:8896
	s_waitcnt lgkmcnt(3)
	v_mfma_f32_32x32x16_f16 v[66:81], v[142:145], v[186:189], v[66:81]
	v_mfma_f32_32x32x16_f16 v[2:17], v[142:145], v[190:193], v[2:17]
	ds_read_b128 v[142:145], v236 offset:13248
	global_load_dwordx4 v[186:189], v239, s[56:57]
	global_load_dwordx4 v[190:193], v239, s[56:57] offset:512
	s_add_u32 s56, s56, 0x4000
	s_addc_u32 s57, s57, 0
	s_waitcnt vmcnt(19)
	v_cvt_pk_f16_f32 v204, v204, v205
	v_cvt_pk_f16_f32 v205, v206, v207
	ds_write_b64 v237, v[204:205] offset:34816
	s_waitcnt vmcnt(18)
	v_cvt_pk_f16_f32 v208, v208, v209
	v_cvt_pk_f16_f32 v209, v210, v211
	ds_write_b64 v237, v[208:209] offset:39168
	s_waitcnt vmcnt(17)
	v_cvt_pk_f16_f32 v212, v212, v213
	v_cvt_pk_f16_f32 v213, v214, v215
	ds_write_b64 v237, v[212:213] offset:43520
	s_waitcnt vmcnt(16)
	v_cvt_pk_f16_f32 v216, v216, v217
	v_cvt_pk_f16_f32 v217, v218, v219
	ds_write_b64 v237, v[216:217] offset:47872
	s_waitcnt vmcnt(15)
	v_cvt_pk_f16_f32 v220, v220, v221
	v_cvt_pk_f16_f32 v221, v222, v223
	ds_write_b64 v237, v[220:221] offset:52224
	s_waitcnt vmcnt(14)
	v_cvt_pk_f16_f32 v224, v224, v225
	v_cvt_pk_f16_f32 v225, v226, v227
	ds_write_b64 v237, v[224:225] offset:56576
	s_waitcnt vmcnt(13)
	v_cvt_pk_f16_f32 v228, v228, v229
	v_cvt_pk_f16_f32 v229, v230, v231
	ds_write_b64 v237, v[228:229] offset:60928
	s_waitcnt vmcnt(12)
	v_cvt_pk_f16_f32 v232, v232, v233
	v_cvt_pk_f16_f32 v233, v234, v235
	ds_write_b64 v237, v[232:233] offset:65280
	global_load_dwordx4 v[204:207], v238, s[40:41] offset:1024
	global_load_dwordx4 v[208:211], v238, s[42:43] offset:1024
	global_load_dwordx4 v[212:215], v238, s[44:45] offset:1024
	global_load_dwordx4 v[216:219], v238, s[46:47] offset:1024
	global_load_dwordx4 v[220:223], v238, s[48:49] offset:1024
	global_load_dwordx4 v[224:227], v238, s[50:51] offset:1024
	global_load_dwordx4 v[228:231], v238, s[52:53] offset:1024
	global_load_dwordx4 v[232:235], v238, s[54:55] offset:1024
	s_waitcnt vmcnt(28)
	s_waitcnt lgkmcnt(11)
	v_mfma_f32_32x32x16_f16 v[82:97], v[130:133], v[194:197], v[82:97]
	v_mfma_f32_32x32x16_f16 v[50:65], v[130:133], v[198:201], v[50:65]
	ds_read_b128 v[130:133], v236 offset:224
	s_waitcnt lgkmcnt(11)
	v_mfma_f32_32x32x16_f16 v[114:129], v[134:137], v[194:197], v[114:129]
	v_mfma_f32_32x32x16_f16 v[34:49], v[134:137], v[198:201], v[34:49]
	ds_read_b128 v[134:137], v236 offset:4576
	s_waitcnt lgkmcnt(11)
	v_mfma_f32_32x32x16_f16 v[98:113], v[138:141], v[194:197], v[98:113]
	v_mfma_f32_32x32x16_f16 v[18:33], v[138:141], v[198:201], v[18:33]
	ds_read_b128 v[138:141], v236 offset:8928
	s_waitcnt lgkmcnt(11)
	v_mfma_f32_32x32x16_f16 v[66:81], v[142:145], v[194:197], v[66:81]
	v_mfma_f32_32x32x16_f16 v[2:17], v[142:145], v[198:201], v[2:17]
	ds_read_b128 v[142:145], v236 offset:13280
	global_load_dwordx4 v[194:197], v239, s[56:57]
	global_load_dwordx4 v[198:201], v239, s[56:57] offset:512
	s_add_u32 s56, s56, 0x4000
	s_addc_u32 s57, s57, 0
	s_waitcnt vmcnt(20)
	s_waitcnt lgkmcnt(3)
	v_mfma_f32_32x32x16_f16 v[82:97], v[130:133], v[146:149], v[82:97]
	v_mfma_f32_32x32x16_f16 v[50:65], v[130:133], v[150:153], v[50:65]
	s_waitcnt lgkmcnt(2)
	v_mfma_f32_32x32x16_f16 v[114:129], v[134:137], v[146:149], v[114:129]
	v_mfma_f32_32x32x16_f16 v[34:49], v[134:137], v[150:153], v[34:49]
	s_waitcnt lgkmcnt(1)
	v_mfma_f32_32x32x16_f16 v[98:113], v[138:141], v[146:149], v[98:113]
	v_mfma_f32_32x32x16_f16 v[18:33], v[138:141], v[150:153], v[18:33]
	s_waitcnt lgkmcnt(0)
	v_mfma_f32_32x32x16_f16 v[66:81], v[142:145], v[146:149], v[66:81]
	v_mfma_f32_32x32x16_f16 v[2:17], v[142:145], v[150:153], v[2:17]
	global_load_dwordx4 v[146:149], v239, s[56:57]
	global_load_dwordx4 v[150:153], v239, s[56:57] offset:512
	s_add_u32 s56, s56, 0x4000
	s_addc_u32 s57, s57, 0
	s_waitcnt lgkmcnt(0)
	s_barrier
	ds_read_b128 v[130:133], v236 offset:34816
	ds_read_b128 v[134:137], v236 offset:39168
	ds_read_b128 v[138:141], v236 offset:43520
	ds_read_b128 v[142:145], v236 offset:47872
	s_waitcnt vmcnt(20)
	s_waitcnt lgkmcnt(3)
	v_mfma_f32_32x32x16_f16 v[82:97], v[130:133], v[154:157], v[82:97]
	v_mfma_f32_32x32x16_f16 v[50:65], v[130:133], v[158:161], v[50:65]
	ds_read_b128 v[130:133], v236 offset:34848
	s_waitcnt lgkmcnt(3)
	v_mfma_f32_32x32x16_f16 v[114:129], v[134:137], v[154:157], v[114:129]
	v_mfma_f32_32x32x16_f16 v[34:49], v[134:137], v[158:161], v[34:49]
	ds_read_b128 v[134:137], v236 offset:39200
	s_waitcnt lgkmcnt(3)
	v_mfma_f32_32x32x16_f16 v[98:113], v[138:141], v[154:157], v[98:113]
	v_mfma_f32_32x32x16_f16 v[18:33], v[138:141], v[158:161], v[18:33]
	ds_read_b128 v[138:141], v236 offset:43552
	s_waitcnt lgkmcnt(3)
	v_mfma_f32_32x32x16_f16 v[66:81], v[142:145], v[154:157], v[66:81]
	v_mfma_f32_32x32x16_f16 v[2:17], v[142:145], v[158:161], v[2:17]
	ds_read_b128 v[142:145], v236 offset:47904
	global_load_dwordx4 v[154:157], v239, s[56:57]
	global_load_dwordx4 v[158:161], v239, s[56:57] offset:512
	s_add_u32 s56, s56, 0x4000
	s_addc_u32 s57, s57, 0
	s_waitcnt vmcnt(20)
	s_waitcnt lgkmcnt(3)
	v_mfma_f32_32x32x16_f16 v[82:97], v[130:133], v[162:165], v[82:97]
	v_mfma_f32_32x32x16_f16 v[50:65], v[130:133], v[166:169], v[50:65]
	ds_read_b128 v[130:133], v236 offset:34880
	s_waitcnt lgkmcnt(3)
	v_mfma_f32_32x32x16_f16 v[114:129], v[134:137], v[162:165], v[114:129]
	v_mfma_f32_32x32x16_f16 v[34:49], v[134:137], v[166:169], v[34:49]
	ds_read_b128 v[134:137], v236 offset:39232
	s_waitcnt lgkmcnt(3)
	v_mfma_f32_32x32x16_f16 v[98:113], v[138:141], v[162:165], v[98:113]
	v_mfma_f32_32x32x16_f16 v[18:33], v[138:141], v[166:169], v[18:33]
	ds_read_b128 v[138:141], v236 offset:43584
	s_waitcnt lgkmcnt(3)
	v_mfma_f32_32x32x16_f16 v[66:81], v[142:145], v[162:165], v[66:81]
	v_mfma_f32_32x32x16_f16 v[2:17], v[142:145], v[166:169], v[2:17]
	ds_read_b128 v[142:145], v236 offset:47936
	global_load_dwordx4 v[162:165], v239, s[56:57]
	global_load_dwordx4 v[166:169], v239, s[56:57] offset:512
	s_add_u32 s56, s56, 0x4000
	s_addc_u32 s57, s57, 0
	s_waitcnt vmcnt(20)
	s_waitcnt lgkmcnt(3)
	v_mfma_f32_32x32x16_f16 v[82:97], v[130:133], v[170:173], v[82:97]
	v_mfma_f32_32x32x16_f16 v[50:65], v[130:133], v[174:177], v[50:65]
	ds_read_b128 v[130:133], v236 offset:34912
	s_waitcnt lgkmcnt(3)
	v_mfma_f32_32x32x16_f16 v[114:129], v[134:137], v[170:173], v[114:129]
	v_mfma_f32_32x32x16_f16 v[34:49], v[134:137], v[174:177], v[34:49]
	ds_read_b128 v[134:137], v236 offset:39264
	s_waitcnt lgkmcnt(3)
	v_mfma_f32_32x32x16_f16 v[98:113], v[138:141], v[170:173], v[98:113]
	v_mfma_f32_32x32x16_f16 v[18:33], v[138:141], v[174:177], v[18:33]
	ds_read_b128 v[138:141], v236 offset:43616
	s_waitcnt lgkmcnt(3)
	v_mfma_f32_32x32x16_f16 v[66:81], v[142:145], v[170:173], v[66:81]
	v_mfma_f32_32x32x16_f16 v[2:17], v[142:145], v[174:177], v[2:17]
	ds_read_b128 v[142:145], v236 offset:47968
	global_load_dwordx4 v[170:173], v239, s[56:57]
	global_load_dwordx4 v[174:177], v239, s[56:57] offset:512
	s_add_u32 s56, s56, 0x4000
	s_addc_u32 s57, s57, 0
	s_waitcnt vmcnt(20)
	s_waitcnt lgkmcnt(3)
	v_mfma_f32_32x32x16_f16 v[82:97], v[130:133], v[178:181], v[82:97]
	v_mfma_f32_32x32x16_f16 v[50:65], v[130:133], v[182:185], v[50:65]
	ds_read_b128 v[130:133], v236 offset:34944
	s_waitcnt lgkmcnt(3)
	v_mfma_f32_32x32x16_f16 v[114:129], v[134:137], v[178:181], v[114:129]
	v_mfma_f32_32x32x16_f16 v[34:49], v[134:137], v[182:185], v[34:49]
	ds_read_b128 v[134:137], v236 offset:39296
	s_waitcnt lgkmcnt(3)
	v_mfma_f32_32x32x16_f16 v[98:113], v[138:141], v[178:181], v[98:113]
	v_mfma_f32_32x32x16_f16 v[18:33], v[138:141], v[182:185], v[18:33]
	ds_read_b128 v[138:141], v236 offset:43648
	s_waitcnt lgkmcnt(3)
	v_mfma_f32_32x32x16_f16 v[66:81], v[142:145], v[178:181], v[66:81]
	v_mfma_f32_32x32x16_f16 v[2:17], v[142:145], v[182:185], v[2:17]
	ds_read_b128 v[142:145], v236 offset:48000
	global_load_dwordx4 v[178:181], v239, s[56:57]
	global_load_dwordx4 v[182:185], v239, s[56:57] offset:512
	s_add_u32 s56, s56, 0x4000
	s_addc_u32 s57, s57, 0
	s_waitcnt vmcnt(20)
	s_waitcnt lgkmcnt(3)
	v_mfma_f32_32x32x16_f16 v[82:97], v[130:133], v[186:189], v[82:97]
	v_mfma_f32_32x32x16_f16 v[50:65], v[130:133], v[190:193], v[50:65]
	ds_read_b128 v[130:133], v236 offset:34976
	s_waitcnt lgkmcnt(3)
	v_mfma_f32_32x32x16_f16 v[114:129], v[134:137], v[186:189], v[114:129]
	v_mfma_f32_32x32x16_f16 v[34:49], v[134:137], v[190:193], v[34:49]
	ds_read_b128 v[134:137], v236 offset:39328
	s_waitcnt lgkmcnt(3)
	v_mfma_f32_32x32x16_f16 v[98:113], v[138:141], v[186:189], v[98:113]
	v_mfma_f32_32x32x16_f16 v[18:33], v[138:141], v[190:193], v[18:33]
	ds_read_b128 v[138:141], v236 offset:43680
	s_waitcnt lgkmcnt(3)
	v_mfma_f32_32x32x16_f16 v[66:81], v[142:145], v[186:189], v[66:81]
	v_mfma_f32_32x32x16_f16 v[2:17], v[142:145], v[190:193], v[2:17]
	ds_read_b128 v[142:145], v236 offset:48032
	global_load_dwordx4 v[186:189], v239, s[56:57]
	global_load_dwordx4 v[190:193], v239, s[56:57] offset:512
	s_add_u32 s56, s56, 0x4000
	s_addc_u32 s57, s57, 0
	s_waitcnt vmcnt(12)
	s_waitcnt lgkmcnt(3)
	v_mfma_f32_32x32x16_f16 v[82:97], v[130:133], v[194:197], v[82:97]
	v_mfma_f32_32x32x16_f16 v[50:65], v[130:133], v[198:201], v[50:65]
	ds_read_b128 v[130:133], v236 offset:35008
	s_waitcnt lgkmcnt(3)
	v_mfma_f32_32x32x16_f16 v[114:129], v[134:137], v[194:197], v[114:129]
	v_mfma_f32_32x32x16_f16 v[34:49], v[134:137], v[198:201], v[34:49]
	ds_read_b128 v[134:137], v236 offset:39360
	s_waitcnt lgkmcnt(3)
	v_mfma_f32_32x32x16_f16 v[98:113], v[138:141], v[194:197], v[98:113]
	v_mfma_f32_32x32x16_f16 v[18:33], v[138:141], v[198:201], v[18:33]
	ds_read_b128 v[138:141], v236 offset:43712
	s_waitcnt lgkmcnt(3)
	v_mfma_f32_32x32x16_f16 v[66:81], v[142:145], v[194:197], v[66:81]
	v_mfma_f32_32x32x16_f16 v[2:17], v[142:145], v[198:201], v[2:17]
	ds_read_b128 v[142:145], v236 offset:48064
	global_load_dwordx4 v[194:197], v239, s[56:57]
	global_load_dwordx4 v[198:201], v239, s[56:57] offset:512
	s_add_u32 s56, s56, 0x4000
	s_addc_u32 s57, s57, 0
	s_waitcnt vmcnt(23)
	v_cvt_pk_f16_f32 v204, v204, v205
	v_cvt_pk_f16_f32 v205, v206, v207
	ds_write_b64 v237, v[204:205]
	s_waitcnt vmcnt(22)
	v_cvt_pk_f16_f32 v208, v208, v209
	v_cvt_pk_f16_f32 v209, v210, v211
	ds_write_b64 v237, v[208:209] offset:4352
	s_waitcnt vmcnt(21)
	v_cvt_pk_f16_f32 v212, v212, v213
	v_cvt_pk_f16_f32 v213, v214, v215
	ds_write_b64 v237, v[212:213] offset:8704
	s_waitcnt vmcnt(20)
	v_cvt_pk_f16_f32 v216, v216, v217
	v_cvt_pk_f16_f32 v217, v218, v219
	ds_write_b64 v237, v[216:217] offset:13056
	s_waitcnt vmcnt(19)
	v_cvt_pk_f16_f32 v220, v220, v221
	v_cvt_pk_f16_f32 v221, v222, v223
	ds_write_b64 v237, v[220:221] offset:17408
	s_waitcnt vmcnt(18)
	v_cvt_pk_f16_f32 v224, v224, v225
	v_cvt_pk_f16_f32 v225, v226, v227
	ds_write_b64 v237, v[224:225] offset:21760
	s_waitcnt vmcnt(17)
	v_cvt_pk_f16_f32 v228, v228, v229
	v_cvt_pk_f16_f32 v229, v230, v231
	ds_write_b64 v237, v[228:229] offset:26112
	s_waitcnt vmcnt(16)
	v_cvt_pk_f16_f32 v232, v232, v233
	v_cvt_pk_f16_f32 v233, v234, v235
	ds_write_b64 v237, v[232:233] offset:30464
	global_load_dwordx4 v[204:207], v238, s[40:41] offset:1536
	global_load_dwordx4 v[208:211], v238, s[42:43] offset:1536
	global_load_dwordx4 v[212:215], v238, s[44:45] offset:1536
	global_load_dwordx4 v[216:219], v238, s[46:47] offset:1536
	global_load_dwordx4 v[220:223], v238, s[48:49] offset:1536
	global_load_dwordx4 v[224:227], v238, s[50:51] offset:1536
	global_load_dwordx4 v[228:231], v238, s[52:53] offset:1536
	global_load_dwordx4 v[232:235], v238, s[54:55] offset:1536
	s_waitcnt vmcnt(20)
	s_waitcnt lgkmcnt(11)
	v_mfma_f32_32x32x16_f16 v[82:97], v[130:133], v[146:149], v[82:97]
	v_mfma_f32_32x32x16_f16 v[50:65], v[130:133], v[150:153], v[50:65]
	ds_read_b128 v[130:133], v236 offset:35040
	s_waitcnt lgkmcnt(11)
	v_mfma_f32_32x32x16_f16 v[114:129], v[134:137], v[146:149], v[114:129]
	v_mfma_f32_32x32x16_f16 v[34:49], v[134:137], v[150:153], v[34:49]
	ds_read_b128 v[134:137], v236 offset:39392
	s_waitcnt lgkmcnt(11)
	v_mfma_f32_32x32x16_f16 v[98:113], v[138:141], v[146:149], v[98:113]
	v_mfma_f32_32x32x16_f16 v[18:33], v[138:141], v[150:153], v[18:33]
	ds_read_b128 v[138:141], v236 offset:43744
	s_waitcnt lgkmcnt(11)
	v_mfma_f32_32x32x16_f16 v[66:81], v[142:145], v[146:149], v[66:81]
	v_mfma_f32_32x32x16_f16 v[2:17], v[142:145], v[150:153], v[2:17]
	ds_read_b128 v[142:145], v236 offset:48096
	global_load_dwordx4 v[146:149], v239, s[56:57]
	global_load_dwordx4 v[150:153], v239, s[56:57] offset:512
	s_add_u32 s56, s56, 0x4000
	s_addc_u32 s57, s57, 0
	s_waitcnt vmcnt(20)
	s_waitcnt lgkmcnt(3)
	v_mfma_f32_32x32x16_f16 v[82:97], v[130:133], v[154:157], v[82:97]
	v_mfma_f32_32x32x16_f16 v[50:65], v[130:133], v[158:161], v[50:65]
	s_waitcnt lgkmcnt(2)
	v_mfma_f32_32x32x16_f16 v[114:129], v[134:137], v[154:157], v[114:129]
	v_mfma_f32_32x32x16_f16 v[34:49], v[134:137], v[158:161], v[34:49]
	s_waitcnt lgkmcnt(1)
	v_mfma_f32_32x32x16_f16 v[98:113], v[138:141], v[154:157], v[98:113]
	v_mfma_f32_32x32x16_f16 v[18:33], v[138:141], v[158:161], v[18:33]
	s_waitcnt lgkmcnt(0)
	v_mfma_f32_32x32x16_f16 v[66:81], v[142:145], v[154:157], v[66:81]
	v_mfma_f32_32x32x16_f16 v[2:17], v[142:145], v[158:161], v[2:17]
	global_load_dwordx4 v[154:157], v239, s[56:57]
	global_load_dwordx4 v[158:161], v239, s[56:57] offset:512
	s_add_u32 s56, s56, 0x4000
	s_addc_u32 s57, s57, 0
	s_waitcnt lgkmcnt(0)
	s_barrier
	ds_read_b128 v[130:133], v236
	ds_read_b128 v[134:137], v236 offset:4352
	ds_read_b128 v[138:141], v236 offset:8704
	ds_read_b128 v[142:145], v236 offset:13056
	s_waitcnt vmcnt(20)
	s_waitcnt lgkmcnt(3)
	v_mfma_f32_32x32x16_f16 v[82:97], v[130:133], v[162:165], v[82:97]
	v_mfma_f32_32x32x16_f16 v[50:65], v[130:133], v[166:169], v[50:65]
	ds_read_b128 v[130:133], v236 offset:32
	s_waitcnt lgkmcnt(3)
	v_mfma_f32_32x32x16_f16 v[114:129], v[134:137], v[162:165], v[114:129]
	v_mfma_f32_32x32x16_f16 v[34:49], v[134:137], v[166:169], v[34:49]
	ds_read_b128 v[134:137], v236 offset:4384
	s_waitcnt lgkmcnt(3)
	v_mfma_f32_32x32x16_f16 v[98:113], v[138:141], v[162:165], v[98:113]
	v_mfma_f32_32x32x16_f16 v[18:33], v[138:141], v[166:169], v[18:33]
	ds_read_b128 v[138:141], v236 offset:8736
	s_waitcnt lgkmcnt(3)
	v_mfma_f32_32x32x16_f16 v[66:81], v[142:145], v[162:165], v[66:81]
	v_mfma_f32_32x32x16_f16 v[2:17], v[142:145], v[166:169], v[2:17]
	ds_read_b128 v[142:145], v236 offset:13088
	global_load_dwordx4 v[162:165], v239, s[56:57]
	global_load_dwordx4 v[166:169], v239, s[56:57] offset:512
	s_add_u32 s56, s56, 0x4000
	s_addc_u32 s57, s57, 0
	s_waitcnt vmcnt(20)
	s_waitcnt lgkmcnt(3)
	v_mfma_f32_32x32x16_f16 v[82:97], v[130:133], v[170:173], v[82:97]
	v_mfma_f32_32x32x16_f16 v[50:65], v[130:133], v[174:177], v[50:65]
	ds_read_b128 v[130:133], v236 offset:64
	s_waitcnt lgkmcnt(3)
	v_mfma_f32_32x32x16_f16 v[114:129], v[134:137], v[170:173], v[114:129]
	v_mfma_f32_32x32x16_f16 v[34:49], v[134:137], v[174:177], v[34:49]
	ds_read_b128 v[134:137], v236 offset:4416
	s_waitcnt lgkmcnt(3)
	v_mfma_f32_32x32x16_f16 v[98:113], v[138:141], v[170:173], v[98:113]
	v_mfma_f32_32x32x16_f16 v[18:33], v[138:141], v[174:177], v[18:33]
	ds_read_b128 v[138:141], v236 offset:8768
	s_waitcnt lgkmcnt(3)
	v_mfma_f32_32x32x16_f16 v[66:81], v[142:145], v[170:173], v[66:81]
	v_mfma_f32_32x32x16_f16 v[2:17], v[142:145], v[174:177], v[2:17]
	ds_read_b128 v[142:145], v236 offset:13120
	global_load_dwordx4 v[170:173], v239, s[56:57]
	global_load_dwordx4 v[174:177], v239, s[56:57] offset:512
	s_add_u32 s56, s56, 0x4000
	s_addc_u32 s57, s57, 0
	s_waitcnt vmcnt(20)
	s_waitcnt lgkmcnt(3)
	v_mfma_f32_32x32x16_f16 v[82:97], v[130:133], v[178:181], v[82:97]
	v_mfma_f32_32x32x16_f16 v[50:65], v[130:133], v[182:185], v[50:65]
	ds_read_b128 v[130:133], v236 offset:96
	s_waitcnt lgkmcnt(3)
	v_mfma_f32_32x32x16_f16 v[114:129], v[134:137], v[178:181], v[114:129]
	v_mfma_f32_32x32x16_f16 v[34:49], v[134:137], v[182:185], v[34:49]
	ds_read_b128 v[134:137], v236 offset:4448
	s_waitcnt lgkmcnt(3)
	v_mfma_f32_32x32x16_f16 v[98:113], v[138:141], v[178:181], v[98:113]
	v_mfma_f32_32x32x16_f16 v[18:33], v[138:141], v[182:185], v[18:33]
	ds_read_b128 v[138:141], v236 offset:8800
	s_waitcnt lgkmcnt(3)
	v_mfma_f32_32x32x16_f16 v[66:81], v[142:145], v[178:181], v[66:81]
	v_mfma_f32_32x32x16_f16 v[2:17], v[142:145], v[182:185], v[2:17]
	ds_read_b128 v[142:145], v236 offset:13152
	global_load_dwordx4 v[178:181], v239, s[56:57]
	global_load_dwordx4 v[182:185], v239, s[56:57] offset:512
	s_add_u32 s56, s56, 0x4000
	s_addc_u32 s57, s57, 0
	s_waitcnt vmcnt(20)
	s_waitcnt lgkmcnt(3)
	v_mfma_f32_32x32x16_f16 v[82:97], v[130:133], v[186:189], v[82:97]
	v_mfma_f32_32x32x16_f16 v[50:65], v[130:133], v[190:193], v[50:65]
	ds_read_b128 v[130:133], v236 offset:128
	s_waitcnt lgkmcnt(3)
	v_mfma_f32_32x32x16_f16 v[114:129], v[134:137], v[186:189], v[114:129]
	v_mfma_f32_32x32x16_f16 v[34:49], v[134:137], v[190:193], v[34:49]
	ds_read_b128 v[134:137], v236 offset:4480
	s_waitcnt lgkmcnt(3)
	v_mfma_f32_32x32x16_f16 v[98:113], v[138:141], v[186:189], v[98:113]
	v_mfma_f32_32x32x16_f16 v[18:33], v[138:141], v[190:193], v[18:33]
	ds_read_b128 v[138:141], v236 offset:8832
	s_waitcnt lgkmcnt(3)
	v_mfma_f32_32x32x16_f16 v[66:81], v[142:145], v[186:189], v[66:81]
	v_mfma_f32_32x32x16_f16 v[2:17], v[142:145], v[190:193], v[2:17]
	ds_read_b128 v[142:145], v236 offset:13184
	global_load_dwordx4 v[186:189], v239, s[56:57]
	global_load_dwordx4 v[190:193], v239, s[56:57] offset:512
	s_add_u32 s56, s56, 0x4000
	s_addc_u32 s57, s57, 0
	s_waitcnt vmcnt(20)
	s_waitcnt lgkmcnt(3)
	v_mfma_f32_32x32x16_f16 v[82:97], v[130:133], v[194:197], v[82:97]
	v_mfma_f32_32x32x16_f16 v[50:65], v[130:133], v[198:201], v[50:65]
	ds_read_b128 v[130:133], v236 offset:160
	s_waitcnt lgkmcnt(3)
	v_mfma_f32_32x32x16_f16 v[114:129], v[134:137], v[194:197], v[114:129]
	v_mfma_f32_32x32x16_f16 v[34:49], v[134:137], v[198:201], v[34:49]
	ds_read_b128 v[134:137], v236 offset:4512
	s_waitcnt lgkmcnt(3)
	v_mfma_f32_32x32x16_f16 v[98:113], v[138:141], v[194:197], v[98:113]
	v_mfma_f32_32x32x16_f16 v[18:33], v[138:141], v[198:201], v[18:33]
	ds_read_b128 v[138:141], v236 offset:8864
	s_waitcnt lgkmcnt(3)
	v_mfma_f32_32x32x16_f16 v[66:81], v[142:145], v[194:197], v[66:81]
	v_mfma_f32_32x32x16_f16 v[2:17], v[142:145], v[198:201], v[2:17]
	ds_read_b128 v[142:145], v236 offset:13216
	global_load_dwordx4 v[194:197], v239, s[56:57]
	global_load_dwordx4 v[198:201], v239, s[56:57] offset:512
	s_add_u32 s56, s56, 0x4000
	s_addc_u32 s57, s57, 0
	s_waitcnt vmcnt(12)
	s_waitcnt lgkmcnt(3)
	v_mfma_f32_32x32x16_f16 v[82:97], v[130:133], v[146:149], v[82:97]
	v_mfma_f32_32x32x16_f16 v[50:65], v[130:133], v[150:153], v[50:65]
	ds_read_b128 v[130:133], v236 offset:192
	s_waitcnt lgkmcnt(3)
	v_mfma_f32_32x32x16_f16 v[114:129], v[134:137], v[146:149], v[114:129]
	v_mfma_f32_32x32x16_f16 v[34:49], v[134:137], v[150:153], v[34:49]
	ds_read_b128 v[134:137], v236 offset:4544
	s_waitcnt lgkmcnt(3)
	v_mfma_f32_32x32x16_f16 v[98:113], v[138:141], v[146:149], v[98:113]
	v_mfma_f32_32x32x16_f16 v[18:33], v[138:141], v[150:153], v[18:33]
	ds_read_b128 v[138:141], v236 offset:8896
	s_waitcnt lgkmcnt(3)
	v_mfma_f32_32x32x16_f16 v[66:81], v[142:145], v[146:149], v[66:81]
	v_mfma_f32_32x32x16_f16 v[2:17], v[142:145], v[150:153], v[2:17]
	ds_read_b128 v[142:145], v236 offset:13248
	global_load_dwordx4 v[146:149], v239, s[56:57]
	global_load_dwordx4 v[150:153], v239, s[56:57] offset:512
	s_add_u32 s56, s56, 0x4000
	s_addc_u32 s57, s57, 0
	s_waitcnt vmcnt(23)
	v_cvt_pk_f16_f32 v204, v204, v205
	v_cvt_pk_f16_f32 v205, v206, v207
	ds_write_b64 v237, v[204:205] offset:34816
	s_waitcnt vmcnt(22)
	v_cvt_pk_f16_f32 v208, v208, v209
	v_cvt_pk_f16_f32 v209, v210, v211
	ds_write_b64 v237, v[208:209] offset:39168
	s_waitcnt vmcnt(21)
	v_cvt_pk_f16_f32 v212, v212, v213
	v_cvt_pk_f16_f32 v213, v214, v215
	ds_write_b64 v237, v[212:213] offset:43520
	s_waitcnt vmcnt(20)
	v_cvt_pk_f16_f32 v216, v216, v217
	v_cvt_pk_f16_f32 v217, v218, v219
	ds_write_b64 v237, v[216:217] offset:47872
	s_waitcnt vmcnt(19)
	v_cvt_pk_f16_f32 v220, v220, v221
	v_cvt_pk_f16_f32 v221, v222, v223
	ds_write_b64 v237, v[220:221] offset:52224
	s_waitcnt vmcnt(18)
	v_cvt_pk_f16_f32 v224, v224, v225
	v_cvt_pk_f16_f32 v225, v226, v227
	ds_write_b64 v237, v[224:225] offset:56576
	s_waitcnt vmcnt(17)
	v_cvt_pk_f16_f32 v228, v228, v229
	v_cvt_pk_f16_f32 v229, v230, v231
	ds_write_b64 v237, v[228:229] offset:60928
	s_waitcnt vmcnt(16)
	v_cvt_pk_f16_f32 v232, v232, v233
	v_cvt_pk_f16_f32 v233, v234, v235
	ds_write_b64 v237, v[232:233] offset:65280
	global_load_dwordx4 v[204:207], v238, s[40:41] offset:2048
	global_load_dwordx4 v[208:211], v238, s[42:43] offset:2048
	global_load_dwordx4 v[212:215], v238, s[44:45] offset:2048
	global_load_dwordx4 v[216:219], v238, s[46:47] offset:2048
	global_load_dwordx4 v[220:223], v238, s[48:49] offset:2048
	global_load_dwordx4 v[224:227], v238, s[50:51] offset:2048
	global_load_dwordx4 v[228:231], v238, s[52:53] offset:2048
	global_load_dwordx4 v[232:235], v238, s[54:55] offset:2048
	s_waitcnt vmcnt(20)
	s_waitcnt lgkmcnt(11)
	v_mfma_f32_32x32x16_f16 v[82:97], v[130:133], v[154:157], v[82:97]
	v_mfma_f32_32x32x16_f16 v[50:65], v[130:133], v[158:161], v[50:65]
	ds_read_b128 v[130:133], v236 offset:224
	s_waitcnt lgkmcnt(11)
	v_mfma_f32_32x32x16_f16 v[114:129], v[134:137], v[154:157], v[114:129]
	v_mfma_f32_32x32x16_f16 v[34:49], v[134:137], v[158:161], v[34:49]
	ds_read_b128 v[134:137], v236 offset:4576
	s_waitcnt lgkmcnt(11)
	v_mfma_f32_32x32x16_f16 v[98:113], v[138:141], v[154:157], v[98:113]
	v_mfma_f32_32x32x16_f16 v[18:33], v[138:141], v[158:161], v[18:33]
	ds_read_b128 v[138:141], v236 offset:8928
	s_waitcnt lgkmcnt(11)
	v_mfma_f32_32x32x16_f16 v[66:81], v[142:145], v[154:157], v[66:81]
	v_mfma_f32_32x32x16_f16 v[2:17], v[142:145], v[158:161], v[2:17]
	ds_read_b128 v[142:145], v236 offset:13280
	global_load_dwordx4 v[154:157], v239, s[56:57]
	global_load_dwordx4 v[158:161], v239, s[56:57] offset:512
	s_add_u32 s56, s56, 0x4000
	s_addc_u32 s57, s57, 0
	s_waitcnt vmcnt(20)
	s_waitcnt lgkmcnt(3)
	v_mfma_f32_32x32x16_f16 v[82:97], v[130:133], v[162:165], v[82:97]
	v_mfma_f32_32x32x16_f16 v[50:65], v[130:133], v[166:169], v[50:65]
	s_waitcnt lgkmcnt(2)
	v_mfma_f32_32x32x16_f16 v[114:129], v[134:137], v[162:165], v[114:129]
	v_mfma_f32_32x32x16_f16 v[34:49], v[134:137], v[166:169], v[34:49]
	s_waitcnt lgkmcnt(1)
	v_mfma_f32_32x32x16_f16 v[98:113], v[138:141], v[162:165], v[98:113]
	v_mfma_f32_32x32x16_f16 v[18:33], v[138:141], v[166:169], v[18:33]
	s_waitcnt lgkmcnt(0)
	v_mfma_f32_32x32x16_f16 v[66:81], v[142:145], v[162:165], v[66:81]
	v_mfma_f32_32x32x16_f16 v[2:17], v[142:145], v[166:169], v[2:17]
	global_load_dwordx4 v[162:165], v239, s[56:57]
	global_load_dwordx4 v[166:169], v239, s[56:57] offset:512
	s_add_u32 s56, s56, 0x4000
	s_addc_u32 s57, s57, 0
	s_waitcnt lgkmcnt(0)
	s_barrier
	ds_read_b128 v[130:133], v236 offset:34816
	ds_read_b128 v[134:137], v236 offset:39168
	ds_read_b128 v[138:141], v236 offset:43520
	ds_read_b128 v[142:145], v236 offset:47872
	s_waitcnt vmcnt(20)
	s_waitcnt lgkmcnt(3)
	v_mfma_f32_32x32x16_f16 v[82:97], v[130:133], v[170:173], v[82:97]
	v_mfma_f32_32x32x16_f16 v[50:65], v[130:133], v[174:177], v[50:65]
	ds_read_b128 v[130:133], v236 offset:34848
	s_waitcnt lgkmcnt(3)
	v_mfma_f32_32x32x16_f16 v[114:129], v[134:137], v[170:173], v[114:129]
	v_mfma_f32_32x32x16_f16 v[34:49], v[134:137], v[174:177], v[34:49]
	ds_read_b128 v[134:137], v236 offset:39200
	s_waitcnt lgkmcnt(3)
	v_mfma_f32_32x32x16_f16 v[98:113], v[138:141], v[170:173], v[98:113]
	v_mfma_f32_32x32x16_f16 v[18:33], v[138:141], v[174:177], v[18:33]
	ds_read_b128 v[138:141], v236 offset:43552
	s_waitcnt lgkmcnt(3)
	v_mfma_f32_32x32x16_f16 v[66:81], v[142:145], v[170:173], v[66:81]
	v_mfma_f32_32x32x16_f16 v[2:17], v[142:145], v[174:177], v[2:17]
	ds_read_b128 v[142:145], v236 offset:47904
	global_load_dwordx4 v[170:173], v239, s[56:57]
	global_load_dwordx4 v[174:177], v239, s[56:57] offset:512
	s_add_u32 s56, s56, 0x4000
	s_addc_u32 s57, s57, 0
	s_waitcnt vmcnt(20)
	s_waitcnt lgkmcnt(3)
	v_mfma_f32_32x32x16_f16 v[82:97], v[130:133], v[178:181], v[82:97]
	v_mfma_f32_32x32x16_f16 v[50:65], v[130:133], v[182:185], v[50:65]
	ds_read_b128 v[130:133], v236 offset:34880
	s_waitcnt lgkmcnt(3)
	v_mfma_f32_32x32x16_f16 v[114:129], v[134:137], v[178:181], v[114:129]
	v_mfma_f32_32x32x16_f16 v[34:49], v[134:137], v[182:185], v[34:49]
	ds_read_b128 v[134:137], v236 offset:39232
	s_waitcnt lgkmcnt(3)
	v_mfma_f32_32x32x16_f16 v[98:113], v[138:141], v[178:181], v[98:113]
	v_mfma_f32_32x32x16_f16 v[18:33], v[138:141], v[182:185], v[18:33]
	ds_read_b128 v[138:141], v236 offset:43584
	s_waitcnt lgkmcnt(3)
	v_mfma_f32_32x32x16_f16 v[66:81], v[142:145], v[178:181], v[66:81]
	v_mfma_f32_32x32x16_f16 v[2:17], v[142:145], v[182:185], v[2:17]
	ds_read_b128 v[142:145], v236 offset:47936
	global_load_dwordx4 v[178:181], v239, s[56:57]
	global_load_dwordx4 v[182:185], v239, s[56:57] offset:512
	s_add_u32 s56, s56, 0x4000
	s_addc_u32 s57, s57, 0
	s_waitcnt vmcnt(20)
	s_waitcnt lgkmcnt(3)
	v_mfma_f32_32x32x16_f16 v[82:97], v[130:133], v[186:189], v[82:97]
	v_mfma_f32_32x32x16_f16 v[50:65], v[130:133], v[190:193], v[50:65]
	ds_read_b128 v[130:133], v236 offset:34912
	s_waitcnt lgkmcnt(3)
	v_mfma_f32_32x32x16_f16 v[114:129], v[134:137], v[186:189], v[114:129]
	v_mfma_f32_32x32x16_f16 v[34:49], v[134:137], v[190:193], v[34:49]
	ds_read_b128 v[134:137], v236 offset:39264
	s_waitcnt lgkmcnt(3)
	v_mfma_f32_32x32x16_f16 v[98:113], v[138:141], v[186:189], v[98:113]
	v_mfma_f32_32x32x16_f16 v[18:33], v[138:141], v[190:193], v[18:33]
	ds_read_b128 v[138:141], v236 offset:43616
	s_waitcnt lgkmcnt(3)
	v_mfma_f32_32x32x16_f16 v[66:81], v[142:145], v[186:189], v[66:81]
	v_mfma_f32_32x32x16_f16 v[2:17], v[142:145], v[190:193], v[2:17]
	ds_read_b128 v[142:145], v236 offset:47968
	global_load_dwordx4 v[186:189], v239, s[56:57]
	global_load_dwordx4 v[190:193], v239, s[56:57] offset:512
	s_add_u32 s56, s56, 0x4000
	s_addc_u32 s57, s57, 0
	s_waitcnt vmcnt(20)
	s_waitcnt lgkmcnt(3)
	v_mfma_f32_32x32x16_f16 v[82:97], v[130:133], v[194:197], v[82:97]
	v_mfma_f32_32x32x16_f16 v[50:65], v[130:133], v[198:201], v[50:65]
	ds_read_b128 v[130:133], v236 offset:34944
	s_waitcnt lgkmcnt(3)
	v_mfma_f32_32x32x16_f16 v[114:129], v[134:137], v[194:197], v[114:129]
	v_mfma_f32_32x32x16_f16 v[34:49], v[134:137], v[198:201], v[34:49]
	ds_read_b128 v[134:137], v236 offset:39296
	s_waitcnt lgkmcnt(3)
	v_mfma_f32_32x32x16_f16 v[98:113], v[138:141], v[194:197], v[98:113]
	v_mfma_f32_32x32x16_f16 v[18:33], v[138:141], v[198:201], v[18:33]
	ds_read_b128 v[138:141], v236 offset:43648
	s_waitcnt lgkmcnt(3)
	v_mfma_f32_32x32x16_f16 v[66:81], v[142:145], v[194:197], v[66:81]
	v_mfma_f32_32x32x16_f16 v[2:17], v[142:145], v[198:201], v[2:17]
	ds_read_b128 v[142:145], v236 offset:48000
	global_load_dwordx4 v[194:197], v239, s[56:57]
	global_load_dwordx4 v[198:201], v239, s[56:57] offset:512
	s_add_u32 s56, s56, 0x4000
	s_addc_u32 s57, s57, 0
	s_waitcnt vmcnt(20)
	s_waitcnt lgkmcnt(3)
	v_mfma_f32_32x32x16_f16 v[82:97], v[130:133], v[146:149], v[82:97]
	v_mfma_f32_32x32x16_f16 v[50:65], v[130:133], v[150:153], v[50:65]
	ds_read_b128 v[130:133], v236 offset:34976
	s_waitcnt lgkmcnt(3)
	v_mfma_f32_32x32x16_f16 v[114:129], v[134:137], v[146:149], v[114:129]
	v_mfma_f32_32x32x16_f16 v[34:49], v[134:137], v[150:153], v[34:49]
	ds_read_b128 v[134:137], v236 offset:39328
	s_waitcnt lgkmcnt(3)
	v_mfma_f32_32x32x16_f16 v[98:113], v[138:141], v[146:149], v[98:113]
	v_mfma_f32_32x32x16_f16 v[18:33], v[138:141], v[150:153], v[18:33]
	ds_read_b128 v[138:141], v236 offset:43680
	s_waitcnt lgkmcnt(3)
	v_mfma_f32_32x32x16_f16 v[66:81], v[142:145], v[146:149], v[66:81]
	v_mfma_f32_32x32x16_f16 v[2:17], v[142:145], v[150:153], v[2:17]
	ds_read_b128 v[142:145], v236 offset:48032
	global_load_dwordx4 v[146:149], v239, s[56:57]
	global_load_dwordx4 v[150:153], v239, s[56:57] offset:512
	s_add_u32 s56, s56, 0x4000
	s_addc_u32 s57, s57, 0
	s_waitcnt vmcnt(12)
	s_waitcnt lgkmcnt(3)
	v_mfma_f32_32x32x16_f16 v[82:97], v[130:133], v[154:157], v[82:97]
	v_mfma_f32_32x32x16_f16 v[50:65], v[130:133], v[158:161], v[50:65]
	ds_read_b128 v[130:133], v236 offset:35008
	s_waitcnt lgkmcnt(3)
	v_mfma_f32_32x32x16_f16 v[114:129], v[134:137], v[154:157], v[114:129]
	v_mfma_f32_32x32x16_f16 v[34:49], v[134:137], v[158:161], v[34:49]
	ds_read_b128 v[134:137], v236 offset:39360
	s_waitcnt lgkmcnt(3)
	v_mfma_f32_32x32x16_f16 v[98:113], v[138:141], v[154:157], v[98:113]
	v_mfma_f32_32x32x16_f16 v[18:33], v[138:141], v[158:161], v[18:33]
	ds_read_b128 v[138:141], v236 offset:43712
	s_waitcnt lgkmcnt(3)
	v_mfma_f32_32x32x16_f16 v[66:81], v[142:145], v[154:157], v[66:81]
	v_mfma_f32_32x32x16_f16 v[2:17], v[142:145], v[158:161], v[2:17]
	ds_read_b128 v[142:145], v236 offset:48064
	global_load_dwordx4 v[154:157], v239, s[56:57]
	global_load_dwordx4 v[158:161], v239, s[56:57] offset:512
	s_add_u32 s56, s56, 0x4000
	s_addc_u32 s57, s57, 0
	s_waitcnt vmcnt(23)
	v_cvt_pk_f16_f32 v204, v204, v205
	v_cvt_pk_f16_f32 v205, v206, v207
	ds_write_b64 v237, v[204:205]
	s_waitcnt vmcnt(22)
	v_cvt_pk_f16_f32 v208, v208, v209
	v_cvt_pk_f16_f32 v209, v210, v211
	ds_write_b64 v237, v[208:209] offset:4352
	s_waitcnt vmcnt(21)
	v_cvt_pk_f16_f32 v212, v212, v213
	v_cvt_pk_f16_f32 v213, v214, v215
	ds_write_b64 v237, v[212:213] offset:8704
	s_waitcnt vmcnt(20)
	v_cvt_pk_f16_f32 v216, v216, v217
	v_cvt_pk_f16_f32 v217, v218, v219
	ds_write_b64 v237, v[216:217] offset:13056
	s_waitcnt vmcnt(19)
	v_cvt_pk_f16_f32 v220, v220, v221
	v_cvt_pk_f16_f32 v221, v222, v223
	ds_write_b64 v237, v[220:221] offset:17408
	s_waitcnt vmcnt(18)
	v_cvt_pk_f16_f32 v224, v224, v225
	v_cvt_pk_f16_f32 v225, v226, v227
	ds_write_b64 v237, v[224:225] offset:21760
	s_waitcnt vmcnt(17)
	v_cvt_pk_f16_f32 v228, v228, v229
	v_cvt_pk_f16_f32 v229, v230, v231
	ds_write_b64 v237, v[228:229] offset:26112
	s_waitcnt vmcnt(16)
	v_cvt_pk_f16_f32 v232, v232, v233
	v_cvt_pk_f16_f32 v233, v234, v235
	ds_write_b64 v237, v[232:233] offset:30464
	global_load_dwordx4 v[204:207], v238, s[40:41] offset:2560
	global_load_dwordx4 v[208:211], v238, s[42:43] offset:2560
	global_load_dwordx4 v[212:215], v238, s[44:45] offset:2560
	global_load_dwordx4 v[216:219], v238, s[46:47] offset:2560
	global_load_dwordx4 v[220:223], v238, s[48:49] offset:2560
	global_load_dwordx4 v[224:227], v238, s[50:51] offset:2560
	global_load_dwordx4 v[228:231], v238, s[52:53] offset:2560
	global_load_dwordx4 v[232:235], v238, s[54:55] offset:2560
	s_waitcnt vmcnt(20)
	s_waitcnt lgkmcnt(11)
	v_mfma_f32_32x32x16_f16 v[82:97], v[130:133], v[162:165], v[82:97]
	v_mfma_f32_32x32x16_f16 v[50:65], v[130:133], v[166:169], v[50:65]
	ds_read_b128 v[130:133], v236 offset:35040
	s_waitcnt lgkmcnt(11)
	v_mfma_f32_32x32x16_f16 v[114:129], v[134:137], v[162:165], v[114:129]
	v_mfma_f32_32x32x16_f16 v[34:49], v[134:137], v[166:169], v[34:49]
	ds_read_b128 v[134:137], v236 offset:39392
	s_waitcnt lgkmcnt(11)
	v_mfma_f32_32x32x16_f16 v[98:113], v[138:141], v[162:165], v[98:113]
	v_mfma_f32_32x32x16_f16 v[18:33], v[138:141], v[166:169], v[18:33]
	ds_read_b128 v[138:141], v236 offset:43744
	s_waitcnt lgkmcnt(11)
	v_mfma_f32_32x32x16_f16 v[66:81], v[142:145], v[162:165], v[66:81]
	v_mfma_f32_32x32x16_f16 v[2:17], v[142:145], v[166:169], v[2:17]
	ds_read_b128 v[142:145], v236 offset:48096
	global_load_dwordx4 v[162:165], v239, s[56:57]
	global_load_dwordx4 v[166:169], v239, s[56:57] offset:512
	s_add_u32 s56, s56, 0x4000
	s_addc_u32 s57, s57, 0
	s_waitcnt vmcnt(20)
	s_waitcnt lgkmcnt(3)
	v_mfma_f32_32x32x16_f16 v[82:97], v[130:133], v[170:173], v[82:97]
	v_mfma_f32_32x32x16_f16 v[50:65], v[130:133], v[174:177], v[50:65]
	s_waitcnt lgkmcnt(2)
	v_mfma_f32_32x32x16_f16 v[114:129], v[134:137], v[170:173], v[114:129]
	v_mfma_f32_32x32x16_f16 v[34:49], v[134:137], v[174:177], v[34:49]
	s_waitcnt lgkmcnt(1)
	v_mfma_f32_32x32x16_f16 v[98:113], v[138:141], v[170:173], v[98:113]
	v_mfma_f32_32x32x16_f16 v[18:33], v[138:141], v[174:177], v[18:33]
	s_waitcnt lgkmcnt(0)
	v_mfma_f32_32x32x16_f16 v[66:81], v[142:145], v[170:173], v[66:81]
	v_mfma_f32_32x32x16_f16 v[2:17], v[142:145], v[174:177], v[2:17]
	global_load_dwordx4 v[170:173], v239, s[56:57]
	global_load_dwordx4 v[174:177], v239, s[56:57] offset:512
	s_add_u32 s56, s56, 0x4000
	s_addc_u32 s57, s57, 0
	s_waitcnt lgkmcnt(0)
	s_barrier
	ds_read_b128 v[130:133], v236
	ds_read_b128 v[134:137], v236 offset:4352
	ds_read_b128 v[138:141], v236 offset:8704
	ds_read_b128 v[142:145], v236 offset:13056
	s_waitcnt vmcnt(20)
	s_waitcnt lgkmcnt(3)
	v_mfma_f32_32x32x16_f16 v[82:97], v[130:133], v[178:181], v[82:97]
	v_mfma_f32_32x32x16_f16 v[50:65], v[130:133], v[182:185], v[50:65]
	ds_read_b128 v[130:133], v236 offset:32
	s_waitcnt lgkmcnt(3)
	v_mfma_f32_32x32x16_f16 v[114:129], v[134:137], v[178:181], v[114:129]
	v_mfma_f32_32x32x16_f16 v[34:49], v[134:137], v[182:185], v[34:49]
	ds_read_b128 v[134:137], v236 offset:4384
	s_waitcnt lgkmcnt(3)
	v_mfma_f32_32x32x16_f16 v[98:113], v[138:141], v[178:181], v[98:113]
	v_mfma_f32_32x32x16_f16 v[18:33], v[138:141], v[182:185], v[18:33]
	ds_read_b128 v[138:141], v236 offset:8736
	s_waitcnt lgkmcnt(3)
	v_mfma_f32_32x32x16_f16 v[66:81], v[142:145], v[178:181], v[66:81]
	v_mfma_f32_32x32x16_f16 v[2:17], v[142:145], v[182:185], v[2:17]
	ds_read_b128 v[142:145], v236 offset:13088
	global_load_dwordx4 v[178:181], v239, s[56:57]
	global_load_dwordx4 v[182:185], v239, s[56:57] offset:512
	s_add_u32 s56, s56, 0x4000
	s_addc_u32 s57, s57, 0
	s_waitcnt vmcnt(20)
	s_waitcnt lgkmcnt(3)
	v_mfma_f32_32x32x16_f16 v[82:97], v[130:133], v[186:189], v[82:97]
	v_mfma_f32_32x32x16_f16 v[50:65], v[130:133], v[190:193], v[50:65]
	ds_read_b128 v[130:133], v236 offset:64
	s_waitcnt lgkmcnt(3)
	v_mfma_f32_32x32x16_f16 v[114:129], v[134:137], v[186:189], v[114:129]
	v_mfma_f32_32x32x16_f16 v[34:49], v[134:137], v[190:193], v[34:49]
	ds_read_b128 v[134:137], v236 offset:4416
	s_waitcnt lgkmcnt(3)
	v_mfma_f32_32x32x16_f16 v[98:113], v[138:141], v[186:189], v[98:113]
	v_mfma_f32_32x32x16_f16 v[18:33], v[138:141], v[190:193], v[18:33]
	ds_read_b128 v[138:141], v236 offset:8768
	s_waitcnt lgkmcnt(3)
	v_mfma_f32_32x32x16_f16 v[66:81], v[142:145], v[186:189], v[66:81]
	v_mfma_f32_32x32x16_f16 v[2:17], v[142:145], v[190:193], v[2:17]
	ds_read_b128 v[142:145], v236 offset:13120
	global_load_dwordx4 v[186:189], v239, s[56:57]
	global_load_dwordx4 v[190:193], v239, s[56:57] offset:512
	s_add_u32 s56, s56, 0x4000
	s_addc_u32 s57, s57, 0
	s_waitcnt vmcnt(20)
	s_waitcnt lgkmcnt(3)
	v_mfma_f32_32x32x16_f16 v[82:97], v[130:133], v[194:197], v[82:97]
	v_mfma_f32_32x32x16_f16 v[50:65], v[130:133], v[198:201], v[50:65]
	ds_read_b128 v[130:133], v236 offset:96
	s_waitcnt lgkmcnt(3)
	v_mfma_f32_32x32x16_f16 v[114:129], v[134:137], v[194:197], v[114:129]
	v_mfma_f32_32x32x16_f16 v[34:49], v[134:137], v[198:201], v[34:49]
	ds_read_b128 v[134:137], v236 offset:4448
	s_waitcnt lgkmcnt(3)
	v_mfma_f32_32x32x16_f16 v[98:113], v[138:141], v[194:197], v[98:113]
	v_mfma_f32_32x32x16_f16 v[18:33], v[138:141], v[198:201], v[18:33]
	ds_read_b128 v[138:141], v236 offset:8800
	s_waitcnt lgkmcnt(3)
	v_mfma_f32_32x32x16_f16 v[66:81], v[142:145], v[194:197], v[66:81]
	v_mfma_f32_32x32x16_f16 v[2:17], v[142:145], v[198:201], v[2:17]
	ds_read_b128 v[142:145], v236 offset:13152
	global_load_dwordx4 v[194:197], v239, s[56:57]
	global_load_dwordx4 v[198:201], v239, s[56:57] offset:512
	s_add_u32 s56, s56, 0x4000
	s_addc_u32 s57, s57, 0
	s_waitcnt vmcnt(20)
	s_waitcnt lgkmcnt(3)
	v_mfma_f32_32x32x16_f16 v[82:97], v[130:133], v[146:149], v[82:97]
	v_mfma_f32_32x32x16_f16 v[50:65], v[130:133], v[150:153], v[50:65]
	ds_read_b128 v[130:133], v236 offset:128
	s_waitcnt lgkmcnt(3)
	v_mfma_f32_32x32x16_f16 v[114:129], v[134:137], v[146:149], v[114:129]
	v_mfma_f32_32x32x16_f16 v[34:49], v[134:137], v[150:153], v[34:49]
	ds_read_b128 v[134:137], v236 offset:4480
	s_waitcnt lgkmcnt(3)
	v_mfma_f32_32x32x16_f16 v[98:113], v[138:141], v[146:149], v[98:113]
	v_mfma_f32_32x32x16_f16 v[18:33], v[138:141], v[150:153], v[18:33]
	ds_read_b128 v[138:141], v236 offset:8832
	s_waitcnt lgkmcnt(3)
	v_mfma_f32_32x32x16_f16 v[66:81], v[142:145], v[146:149], v[66:81]
	v_mfma_f32_32x32x16_f16 v[2:17], v[142:145], v[150:153], v[2:17]
	ds_read_b128 v[142:145], v236 offset:13184
	global_load_dwordx4 v[146:149], v239, s[56:57]
	global_load_dwordx4 v[150:153], v239, s[56:57] offset:512
	s_add_u32 s56, s56, 0x4000
	s_addc_u32 s57, s57, 0
	s_waitcnt vmcnt(20)
	s_waitcnt lgkmcnt(3)
	v_mfma_f32_32x32x16_f16 v[82:97], v[130:133], v[154:157], v[82:97]
	v_mfma_f32_32x32x16_f16 v[50:65], v[130:133], v[158:161], v[50:65]
	ds_read_b128 v[130:133], v236 offset:160
	s_waitcnt lgkmcnt(3)
	v_mfma_f32_32x32x16_f16 v[114:129], v[134:137], v[154:157], v[114:129]
	v_mfma_f32_32x32x16_f16 v[34:49], v[134:137], v[158:161], v[34:49]
	ds_read_b128 v[134:137], v236 offset:4512
	s_waitcnt lgkmcnt(3)
	v_mfma_f32_32x32x16_f16 v[98:113], v[138:141], v[154:157], v[98:113]
	v_mfma_f32_32x32x16_f16 v[18:33], v[138:141], v[158:161], v[18:33]
	ds_read_b128 v[138:141], v236 offset:8864
	s_waitcnt lgkmcnt(3)
	v_mfma_f32_32x32x16_f16 v[66:81], v[142:145], v[154:157], v[66:81]
	v_mfma_f32_32x32x16_f16 v[2:17], v[142:145], v[158:161], v[2:17]
	ds_read_b128 v[142:145], v236 offset:13216
	global_load_dwordx4 v[154:157], v239, s[56:57]
	global_load_dwordx4 v[158:161], v239, s[56:57] offset:512
	s_add_u32 s56, s56, 0x4000
	s_addc_u32 s57, s57, 0
	s_waitcnt vmcnt(12)
	s_waitcnt lgkmcnt(3)
	v_mfma_f32_32x32x16_f16 v[82:97], v[130:133], v[162:165], v[82:97]
	v_mfma_f32_32x32x16_f16 v[50:65], v[130:133], v[166:169], v[50:65]
	ds_read_b128 v[130:133], v236 offset:192
	s_waitcnt lgkmcnt(3)
	v_mfma_f32_32x32x16_f16 v[114:129], v[134:137], v[162:165], v[114:129]
	v_mfma_f32_32x32x16_f16 v[34:49], v[134:137], v[166:169], v[34:49]
	ds_read_b128 v[134:137], v236 offset:4544
	s_waitcnt lgkmcnt(3)
	v_mfma_f32_32x32x16_f16 v[98:113], v[138:141], v[162:165], v[98:113]
	v_mfma_f32_32x32x16_f16 v[18:33], v[138:141], v[166:169], v[18:33]
	ds_read_b128 v[138:141], v236 offset:8896
	s_waitcnt lgkmcnt(3)
	v_mfma_f32_32x32x16_f16 v[66:81], v[142:145], v[162:165], v[66:81]
	v_mfma_f32_32x32x16_f16 v[2:17], v[142:145], v[166:169], v[2:17]
	ds_read_b128 v[142:145], v236 offset:13248
	global_load_dwordx4 v[162:165], v239, s[56:57]
	global_load_dwordx4 v[166:169], v239, s[56:57] offset:512
	s_add_u32 s56, s56, 0x4000
	s_addc_u32 s57, s57, 0
	s_waitcnt vmcnt(23)
	v_cvt_pk_f16_f32 v204, v204, v205
	v_cvt_pk_f16_f32 v205, v206, v207
	ds_write_b64 v237, v[204:205] offset:34816
	s_waitcnt vmcnt(22)
	v_cvt_pk_f16_f32 v208, v208, v209
	v_cvt_pk_f16_f32 v209, v210, v211
	ds_write_b64 v237, v[208:209] offset:39168
	s_waitcnt vmcnt(21)
	v_cvt_pk_f16_f32 v212, v212, v213
	v_cvt_pk_f16_f32 v213, v214, v215
	ds_write_b64 v237, v[212:213] offset:43520
	s_waitcnt vmcnt(20)
	v_cvt_pk_f16_f32 v216, v216, v217
	v_cvt_pk_f16_f32 v217, v218, v219
	ds_write_b64 v237, v[216:217] offset:47872
	s_waitcnt vmcnt(19)
	v_cvt_pk_f16_f32 v220, v220, v221
	v_cvt_pk_f16_f32 v221, v222, v223
	ds_write_b64 v237, v[220:221] offset:52224
	s_waitcnt vmcnt(18)
	v_cvt_pk_f16_f32 v224, v224, v225
	v_cvt_pk_f16_f32 v225, v226, v227
	ds_write_b64 v237, v[224:225] offset:56576
	s_waitcnt vmcnt(17)
	v_cvt_pk_f16_f32 v228, v228, v229
	v_cvt_pk_f16_f32 v229, v230, v231
	ds_write_b64 v237, v[228:229] offset:60928
	s_waitcnt vmcnt(16)
	v_cvt_pk_f16_f32 v232, v232, v233
	v_cvt_pk_f16_f32 v233, v234, v235
	ds_write_b64 v237, v[232:233] offset:65280
	global_load_dwordx4 v[204:207], v238, s[40:41] offset:3072
	global_load_dwordx4 v[208:211], v238, s[42:43] offset:3072
	global_load_dwordx4 v[212:215], v238, s[44:45] offset:3072
	global_load_dwordx4 v[216:219], v238, s[46:47] offset:3072
	global_load_dwordx4 v[220:223], v238, s[48:49] offset:3072
	global_load_dwordx4 v[224:227], v238, s[50:51] offset:3072
	global_load_dwordx4 v[228:231], v238, s[52:53] offset:3072
	global_load_dwordx4 v[232:235], v238, s[54:55] offset:3072
	s_waitcnt vmcnt(20)
	s_waitcnt lgkmcnt(11)
	v_mfma_f32_32x32x16_f16 v[82:97], v[130:133], v[170:173], v[82:97]
	v_mfma_f32_32x32x16_f16 v[50:65], v[130:133], v[174:177], v[50:65]
	ds_read_b128 v[130:133], v236 offset:224
	s_waitcnt lgkmcnt(11)
	v_mfma_f32_32x32x16_f16 v[114:129], v[134:137], v[170:173], v[114:129]
	v_mfma_f32_32x32x16_f16 v[34:49], v[134:137], v[174:177], v[34:49]
	ds_read_b128 v[134:137], v236 offset:4576
	s_waitcnt lgkmcnt(11)
	v_mfma_f32_32x32x16_f16 v[98:113], v[138:141], v[170:173], v[98:113]
	v_mfma_f32_32x32x16_f16 v[18:33], v[138:141], v[174:177], v[18:33]
	ds_read_b128 v[138:141], v236 offset:8928
	s_waitcnt lgkmcnt(11)
	v_mfma_f32_32x32x16_f16 v[66:81], v[142:145], v[170:173], v[66:81]
	v_mfma_f32_32x32x16_f16 v[2:17], v[142:145], v[174:177], v[2:17]
	ds_read_b128 v[142:145], v236 offset:13280
	global_load_dwordx4 v[170:173], v239, s[56:57]
	global_load_dwordx4 v[174:177], v239, s[56:57] offset:512
	s_add_u32 s56, s56, 0x4000
	s_addc_u32 s57, s57, 0
	s_waitcnt vmcnt(20)
	s_waitcnt lgkmcnt(3)
	v_mfma_f32_32x32x16_f16 v[82:97], v[130:133], v[178:181], v[82:97]
	v_mfma_f32_32x32x16_f16 v[50:65], v[130:133], v[182:185], v[50:65]
	s_waitcnt lgkmcnt(2)
	v_mfma_f32_32x32x16_f16 v[114:129], v[134:137], v[178:181], v[114:129]
	v_mfma_f32_32x32x16_f16 v[34:49], v[134:137], v[182:185], v[34:49]
	s_waitcnt lgkmcnt(1)
	v_mfma_f32_32x32x16_f16 v[98:113], v[138:141], v[178:181], v[98:113]
	v_mfma_f32_32x32x16_f16 v[18:33], v[138:141], v[182:185], v[18:33]
	s_waitcnt lgkmcnt(0)
	v_mfma_f32_32x32x16_f16 v[66:81], v[142:145], v[178:181], v[66:81]
	v_mfma_f32_32x32x16_f16 v[2:17], v[142:145], v[182:185], v[2:17]
	global_load_dwordx4 v[178:181], v239, s[56:57]
	global_load_dwordx4 v[182:185], v239, s[56:57] offset:512
	s_add_u32 s56, s56, 0x4000
	s_addc_u32 s57, s57, 0
	s_waitcnt lgkmcnt(0)
	s_barrier
	ds_read_b128 v[130:133], v236 offset:34816
	ds_read_b128 v[134:137], v236 offset:39168
	ds_read_b128 v[138:141], v236 offset:43520
	ds_read_b128 v[142:145], v236 offset:47872
	s_waitcnt vmcnt(20)
	s_waitcnt lgkmcnt(3)
	v_mfma_f32_32x32x16_f16 v[82:97], v[130:133], v[186:189], v[82:97]
	v_mfma_f32_32x32x16_f16 v[50:65], v[130:133], v[190:193], v[50:65]
	ds_read_b128 v[130:133], v236 offset:34848
	s_waitcnt lgkmcnt(3)
	v_mfma_f32_32x32x16_f16 v[114:129], v[134:137], v[186:189], v[114:129]
	v_mfma_f32_32x32x16_f16 v[34:49], v[134:137], v[190:193], v[34:49]
	ds_read_b128 v[134:137], v236 offset:39200
	s_waitcnt lgkmcnt(3)
	v_mfma_f32_32x32x16_f16 v[98:113], v[138:141], v[186:189], v[98:113]
	v_mfma_f32_32x32x16_f16 v[18:33], v[138:141], v[190:193], v[18:33]
	ds_read_b128 v[138:141], v236 offset:43552
	s_waitcnt lgkmcnt(3)
	v_mfma_f32_32x32x16_f16 v[66:81], v[142:145], v[186:189], v[66:81]
	v_mfma_f32_32x32x16_f16 v[2:17], v[142:145], v[190:193], v[2:17]
	ds_read_b128 v[142:145], v236 offset:47904
	global_load_dwordx4 v[186:189], v239, s[56:57]
	global_load_dwordx4 v[190:193], v239, s[56:57] offset:512
	s_add_u32 s56, s56, 0x4000
	s_addc_u32 s57, s57, 0
	s_waitcnt vmcnt(20)
	s_waitcnt lgkmcnt(3)
	v_mfma_f32_32x32x16_f16 v[82:97], v[130:133], v[194:197], v[82:97]
	v_mfma_f32_32x32x16_f16 v[50:65], v[130:133], v[198:201], v[50:65]
	ds_read_b128 v[130:133], v236 offset:34880
	s_waitcnt lgkmcnt(3)
	v_mfma_f32_32x32x16_f16 v[114:129], v[134:137], v[194:197], v[114:129]
	v_mfma_f32_32x32x16_f16 v[34:49], v[134:137], v[198:201], v[34:49]
	ds_read_b128 v[134:137], v236 offset:39232
	s_waitcnt lgkmcnt(3)
	v_mfma_f32_32x32x16_f16 v[98:113], v[138:141], v[194:197], v[98:113]
	v_mfma_f32_32x32x16_f16 v[18:33], v[138:141], v[198:201], v[18:33]
	ds_read_b128 v[138:141], v236 offset:43584
	s_waitcnt lgkmcnt(3)
	v_mfma_f32_32x32x16_f16 v[66:81], v[142:145], v[194:197], v[66:81]
	v_mfma_f32_32x32x16_f16 v[2:17], v[142:145], v[198:201], v[2:17]
	ds_read_b128 v[142:145], v236 offset:47936
	global_load_dwordx4 v[194:197], v239, s[56:57]
	global_load_dwordx4 v[198:201], v239, s[56:57] offset:512
	s_add_u32 s56, s56, 0x4000
	s_addc_u32 s57, s57, 0
	s_waitcnt vmcnt(20)
	s_waitcnt lgkmcnt(3)
	v_mfma_f32_32x32x16_f16 v[82:97], v[130:133], v[146:149], v[82:97]
	v_mfma_f32_32x32x16_f16 v[50:65], v[130:133], v[150:153], v[50:65]
	ds_read_b128 v[130:133], v236 offset:34912
	s_waitcnt lgkmcnt(3)
	v_mfma_f32_32x32x16_f16 v[114:129], v[134:137], v[146:149], v[114:129]
	v_mfma_f32_32x32x16_f16 v[34:49], v[134:137], v[150:153], v[34:49]
	ds_read_b128 v[134:137], v236 offset:39264
	s_waitcnt lgkmcnt(3)
	v_mfma_f32_32x32x16_f16 v[98:113], v[138:141], v[146:149], v[98:113]
	v_mfma_f32_32x32x16_f16 v[18:33], v[138:141], v[150:153], v[18:33]
	ds_read_b128 v[138:141], v236 offset:43616
	s_waitcnt lgkmcnt(3)
	v_mfma_f32_32x32x16_f16 v[66:81], v[142:145], v[146:149], v[66:81]
	v_mfma_f32_32x32x16_f16 v[2:17], v[142:145], v[150:153], v[2:17]
	ds_read_b128 v[142:145], v236 offset:47968
	global_load_dwordx4 v[146:149], v239, s[56:57]
	global_load_dwordx4 v[150:153], v239, s[56:57] offset:512
	s_add_u32 s56, s56, 0x4000
	s_addc_u32 s57, s57, 0
	s_waitcnt vmcnt(20)
	s_waitcnt lgkmcnt(3)
	v_mfma_f32_32x32x16_f16 v[82:97], v[130:133], v[154:157], v[82:97]
	v_mfma_f32_32x32x16_f16 v[50:65], v[130:133], v[158:161], v[50:65]
	ds_read_b128 v[130:133], v236 offset:34944
	s_waitcnt lgkmcnt(3)
	v_mfma_f32_32x32x16_f16 v[114:129], v[134:137], v[154:157], v[114:129]
	v_mfma_f32_32x32x16_f16 v[34:49], v[134:137], v[158:161], v[34:49]
	ds_read_b128 v[134:137], v236 offset:39296
	s_waitcnt lgkmcnt(3)
	v_mfma_f32_32x32x16_f16 v[98:113], v[138:141], v[154:157], v[98:113]
	v_mfma_f32_32x32x16_f16 v[18:33], v[138:141], v[158:161], v[18:33]
	ds_read_b128 v[138:141], v236 offset:43648
	s_waitcnt lgkmcnt(3)
	v_mfma_f32_32x32x16_f16 v[66:81], v[142:145], v[154:157], v[66:81]
	v_mfma_f32_32x32x16_f16 v[2:17], v[142:145], v[158:161], v[2:17]
	ds_read_b128 v[142:145], v236 offset:48000
	global_load_dwordx4 v[154:157], v239, s[56:57]
	global_load_dwordx4 v[158:161], v239, s[56:57] offset:512
	s_add_u32 s56, s56, 0x4000
	s_addc_u32 s57, s57, 0
	s_waitcnt vmcnt(20)
	s_waitcnt lgkmcnt(3)
	v_mfma_f32_32x32x16_f16 v[82:97], v[130:133], v[162:165], v[82:97]
	v_mfma_f32_32x32x16_f16 v[50:65], v[130:133], v[166:169], v[50:65]
	ds_read_b128 v[130:133], v236 offset:34976
	s_waitcnt lgkmcnt(3)
	v_mfma_f32_32x32x16_f16 v[114:129], v[134:137], v[162:165], v[114:129]
	v_mfma_f32_32x32x16_f16 v[34:49], v[134:137], v[166:169], v[34:49]
	ds_read_b128 v[134:137], v236 offset:39328
	s_waitcnt lgkmcnt(3)
	v_mfma_f32_32x32x16_f16 v[98:113], v[138:141], v[162:165], v[98:113]
	v_mfma_f32_32x32x16_f16 v[18:33], v[138:141], v[166:169], v[18:33]
	ds_read_b128 v[138:141], v236 offset:43680
	s_waitcnt lgkmcnt(3)
	v_mfma_f32_32x32x16_f16 v[66:81], v[142:145], v[162:165], v[66:81]
	v_mfma_f32_32x32x16_f16 v[2:17], v[142:145], v[166:169], v[2:17]
	ds_read_b128 v[142:145], v236 offset:48032
	global_load_dwordx4 v[162:165], v239, s[56:57]
	global_load_dwordx4 v[166:169], v239, s[56:57] offset:512
	s_add_u32 s56, s56, 0x4000
	s_addc_u32 s57, s57, 0
	s_waitcnt vmcnt(12)
	s_waitcnt lgkmcnt(3)
	v_mfma_f32_32x32x16_f16 v[82:97], v[130:133], v[170:173], v[82:97]
	v_mfma_f32_32x32x16_f16 v[50:65], v[130:133], v[174:177], v[50:65]
	ds_read_b128 v[130:133], v236 offset:35008
	s_waitcnt lgkmcnt(3)
	v_mfma_f32_32x32x16_f16 v[114:129], v[134:137], v[170:173], v[114:129]
	v_mfma_f32_32x32x16_f16 v[34:49], v[134:137], v[174:177], v[34:49]
	ds_read_b128 v[134:137], v236 offset:39360
	s_waitcnt lgkmcnt(3)
	v_mfma_f32_32x32x16_f16 v[98:113], v[138:141], v[170:173], v[98:113]
	v_mfma_f32_32x32x16_f16 v[18:33], v[138:141], v[174:177], v[18:33]
	ds_read_b128 v[138:141], v236 offset:43712
	s_waitcnt lgkmcnt(3)
	v_mfma_f32_32x32x16_f16 v[66:81], v[142:145], v[170:173], v[66:81]
	v_mfma_f32_32x32x16_f16 v[2:17], v[142:145], v[174:177], v[2:17]
	ds_read_b128 v[142:145], v236 offset:48064
	global_load_dwordx4 v[170:173], v239, s[56:57]
	global_load_dwordx4 v[174:177], v239, s[56:57] offset:512
	s_add_u32 s56, s56, 0x4000
	s_addc_u32 s57, s57, 0
	s_waitcnt vmcnt(23)
	v_cvt_pk_f16_f32 v204, v204, v205
	v_cvt_pk_f16_f32 v205, v206, v207
	ds_write_b64 v237, v[204:205]
	s_waitcnt vmcnt(22)
	v_cvt_pk_f16_f32 v208, v208, v209
	v_cvt_pk_f16_f32 v209, v210, v211
	ds_write_b64 v237, v[208:209] offset:4352
	s_waitcnt vmcnt(21)
	v_cvt_pk_f16_f32 v212, v212, v213
	v_cvt_pk_f16_f32 v213, v214, v215
	ds_write_b64 v237, v[212:213] offset:8704
	s_waitcnt vmcnt(20)
	v_cvt_pk_f16_f32 v216, v216, v217
	v_cvt_pk_f16_f32 v217, v218, v219
	ds_write_b64 v237, v[216:217] offset:13056
	s_waitcnt vmcnt(19)
	v_cvt_pk_f16_f32 v220, v220, v221
	v_cvt_pk_f16_f32 v221, v222, v223
	ds_write_b64 v237, v[220:221] offset:17408
	s_waitcnt vmcnt(18)
	v_cvt_pk_f16_f32 v224, v224, v225
	v_cvt_pk_f16_f32 v225, v226, v227
	ds_write_b64 v237, v[224:225] offset:21760
	s_waitcnt vmcnt(17)
	v_cvt_pk_f16_f32 v228, v228, v229
	v_cvt_pk_f16_f32 v229, v230, v231
	ds_write_b64 v237, v[228:229] offset:26112
	s_waitcnt vmcnt(16)
	v_cvt_pk_f16_f32 v232, v232, v233
	v_cvt_pk_f16_f32 v233, v234, v235
	ds_write_b64 v237, v[232:233] offset:30464
	global_load_dwordx4 v[204:207], v238, s[40:41] offset:3584
	global_load_dwordx4 v[208:211], v238, s[42:43] offset:3584
	global_load_dwordx4 v[212:215], v238, s[44:45] offset:3584
	global_load_dwordx4 v[216:219], v238, s[46:47] offset:3584
	global_load_dwordx4 v[220:223], v238, s[48:49] offset:3584
	global_load_dwordx4 v[224:227], v238, s[50:51] offset:3584
	global_load_dwordx4 v[228:231], v238, s[52:53] offset:3584
	global_load_dwordx4 v[232:235], v238, s[54:55] offset:3584
	s_waitcnt vmcnt(20)
	s_waitcnt lgkmcnt(11)
	v_mfma_f32_32x32x16_f16 v[82:97], v[130:133], v[178:181], v[82:97]
	v_mfma_f32_32x32x16_f16 v[50:65], v[130:133], v[182:185], v[50:65]
	ds_read_b128 v[130:133], v236 offset:35040
	s_waitcnt lgkmcnt(11)
	v_mfma_f32_32x32x16_f16 v[114:129], v[134:137], v[178:181], v[114:129]
	v_mfma_f32_32x32x16_f16 v[34:49], v[134:137], v[182:185], v[34:49]
	ds_read_b128 v[134:137], v236 offset:39392
	s_waitcnt lgkmcnt(11)
	v_mfma_f32_32x32x16_f16 v[98:113], v[138:141], v[178:181], v[98:113]
	v_mfma_f32_32x32x16_f16 v[18:33], v[138:141], v[182:185], v[18:33]
	ds_read_b128 v[138:141], v236 offset:43744
	s_waitcnt lgkmcnt(11)
	v_mfma_f32_32x32x16_f16 v[66:81], v[142:145], v[178:181], v[66:81]
	v_mfma_f32_32x32x16_f16 v[2:17], v[142:145], v[182:185], v[2:17]
	ds_read_b128 v[142:145], v236 offset:48096
	global_load_dwordx4 v[178:181], v239, s[56:57]
	global_load_dwordx4 v[182:185], v239, s[56:57] offset:512
	s_add_u32 s56, s56, 0x4000
	s_addc_u32 s57, s57, 0
	s_waitcnt vmcnt(20)
	s_waitcnt lgkmcnt(3)
	v_mfma_f32_32x32x16_f16 v[82:97], v[130:133], v[186:189], v[82:97]
	v_mfma_f32_32x32x16_f16 v[50:65], v[130:133], v[190:193], v[50:65]
	s_waitcnt lgkmcnt(2)
	v_mfma_f32_32x32x16_f16 v[114:129], v[134:137], v[186:189], v[114:129]
	v_mfma_f32_32x32x16_f16 v[34:49], v[134:137], v[190:193], v[34:49]
	s_waitcnt lgkmcnt(1)
	v_mfma_f32_32x32x16_f16 v[98:113], v[138:141], v[186:189], v[98:113]
	v_mfma_f32_32x32x16_f16 v[18:33], v[138:141], v[190:193], v[18:33]
	s_waitcnt lgkmcnt(0)
	v_mfma_f32_32x32x16_f16 v[66:81], v[142:145], v[186:189], v[66:81]
	v_mfma_f32_32x32x16_f16 v[2:17], v[142:145], v[190:193], v[2:17]
	global_load_dwordx4 v[186:189], v239, s[56:57]
	global_load_dwordx4 v[190:193], v239, s[56:57] offset:512
	s_add_u32 s56, s56, 0x4000
	s_addc_u32 s57, s57, 0
	s_waitcnt lgkmcnt(0)
	s_barrier
	ds_read_b128 v[130:133], v236
	ds_read_b128 v[134:137], v236 offset:4352
	ds_read_b128 v[138:141], v236 offset:8704
	ds_read_b128 v[142:145], v236 offset:13056
	s_waitcnt vmcnt(20)
	s_waitcnt lgkmcnt(3)
	v_mfma_f32_32x32x16_f16 v[82:97], v[130:133], v[194:197], v[82:97]
	v_mfma_f32_32x32x16_f16 v[50:65], v[130:133], v[198:201], v[50:65]
	ds_read_b128 v[130:133], v236 offset:32
	s_waitcnt lgkmcnt(3)
	v_mfma_f32_32x32x16_f16 v[114:129], v[134:137], v[194:197], v[114:129]
	v_mfma_f32_32x32x16_f16 v[34:49], v[134:137], v[198:201], v[34:49]
	ds_read_b128 v[134:137], v236 offset:4384
	s_waitcnt lgkmcnt(3)
	v_mfma_f32_32x32x16_f16 v[98:113], v[138:141], v[194:197], v[98:113]
	v_mfma_f32_32x32x16_f16 v[18:33], v[138:141], v[198:201], v[18:33]
	ds_read_b128 v[138:141], v236 offset:8736
	s_waitcnt lgkmcnt(3)
	v_mfma_f32_32x32x16_f16 v[66:81], v[142:145], v[194:197], v[66:81]
	v_mfma_f32_32x32x16_f16 v[2:17], v[142:145], v[198:201], v[2:17]
	ds_read_b128 v[142:145], v236 offset:13088
	global_load_dwordx4 v[194:197], v239, s[56:57]
	global_load_dwordx4 v[198:201], v239, s[56:57] offset:512
	s_add_u32 s56, s56, 0x4000
	s_addc_u32 s57, s57, 0
	s_waitcnt vmcnt(20)
	s_waitcnt lgkmcnt(3)
	v_mfma_f32_32x32x16_f16 v[82:97], v[130:133], v[146:149], v[82:97]
	v_mfma_f32_32x32x16_f16 v[50:65], v[130:133], v[150:153], v[50:65]
	ds_read_b128 v[130:133], v236 offset:64
	s_waitcnt lgkmcnt(3)
	v_mfma_f32_32x32x16_f16 v[114:129], v[134:137], v[146:149], v[114:129]
	v_mfma_f32_32x32x16_f16 v[34:49], v[134:137], v[150:153], v[34:49]
	ds_read_b128 v[134:137], v236 offset:4416
	s_waitcnt lgkmcnt(3)
	v_mfma_f32_32x32x16_f16 v[98:113], v[138:141], v[146:149], v[98:113]
	v_mfma_f32_32x32x16_f16 v[18:33], v[138:141], v[150:153], v[18:33]
	ds_read_b128 v[138:141], v236 offset:8768
	s_waitcnt lgkmcnt(3)
	v_mfma_f32_32x32x16_f16 v[66:81], v[142:145], v[146:149], v[66:81]
	v_mfma_f32_32x32x16_f16 v[2:17], v[142:145], v[150:153], v[2:17]
	ds_read_b128 v[142:145], v236 offset:13120
	global_load_dwordx4 v[146:149], v239, s[56:57]
	global_load_dwordx4 v[150:153], v239, s[56:57] offset:512
	s_add_u32 s56, s56, 0x4000
	s_addc_u32 s57, s57, 0
	s_waitcnt vmcnt(20)
	s_waitcnt lgkmcnt(3)
	v_mfma_f32_32x32x16_f16 v[82:97], v[130:133], v[154:157], v[82:97]
	v_mfma_f32_32x32x16_f16 v[50:65], v[130:133], v[158:161], v[50:65]
	ds_read_b128 v[130:133], v236 offset:96
	s_waitcnt lgkmcnt(3)
	v_mfma_f32_32x32x16_f16 v[114:129], v[134:137], v[154:157], v[114:129]
	v_mfma_f32_32x32x16_f16 v[34:49], v[134:137], v[158:161], v[34:49]
	ds_read_b128 v[134:137], v236 offset:4448
	s_waitcnt lgkmcnt(3)
	v_mfma_f32_32x32x16_f16 v[98:113], v[138:141], v[154:157], v[98:113]
	v_mfma_f32_32x32x16_f16 v[18:33], v[138:141], v[158:161], v[18:33]
	ds_read_b128 v[138:141], v236 offset:8800
	s_waitcnt lgkmcnt(3)
	v_mfma_f32_32x32x16_f16 v[66:81], v[142:145], v[154:157], v[66:81]
	v_mfma_f32_32x32x16_f16 v[2:17], v[142:145], v[158:161], v[2:17]
	ds_read_b128 v[142:145], v236 offset:13152
	global_load_dwordx4 v[154:157], v239, s[56:57]
	global_load_dwordx4 v[158:161], v239, s[56:57] offset:512
	s_add_u32 s56, s56, 0x4000
	s_addc_u32 s57, s57, 0
	s_waitcnt vmcnt(20)
	s_waitcnt lgkmcnt(3)
	v_mfma_f32_32x32x16_f16 v[82:97], v[130:133], v[162:165], v[82:97]
	v_mfma_f32_32x32x16_f16 v[50:65], v[130:133], v[166:169], v[50:65]
	ds_read_b128 v[130:133], v236 offset:128
	s_waitcnt lgkmcnt(3)
	v_mfma_f32_32x32x16_f16 v[114:129], v[134:137], v[162:165], v[114:129]
	v_mfma_f32_32x32x16_f16 v[34:49], v[134:137], v[166:169], v[34:49]
	ds_read_b128 v[134:137], v236 offset:4480
	s_waitcnt lgkmcnt(3)
	v_mfma_f32_32x32x16_f16 v[98:113], v[138:141], v[162:165], v[98:113]
	v_mfma_f32_32x32x16_f16 v[18:33], v[138:141], v[166:169], v[18:33]
	ds_read_b128 v[138:141], v236 offset:8832
	s_waitcnt lgkmcnt(3)
	v_mfma_f32_32x32x16_f16 v[66:81], v[142:145], v[162:165], v[66:81]
	v_mfma_f32_32x32x16_f16 v[2:17], v[142:145], v[166:169], v[2:17]
	ds_read_b128 v[142:145], v236 offset:13184
	global_load_dwordx4 v[162:165], v239, s[56:57]
	global_load_dwordx4 v[166:169], v239, s[56:57] offset:512
	s_add_u32 s56, s56, 0x4000
	s_addc_u32 s57, s57, 0
	s_waitcnt vmcnt(20)
	s_waitcnt lgkmcnt(3)
	v_mfma_f32_32x32x16_f16 v[82:97], v[130:133], v[170:173], v[82:97]
	v_mfma_f32_32x32x16_f16 v[50:65], v[130:133], v[174:177], v[50:65]
	ds_read_b128 v[130:133], v236 offset:160
	s_waitcnt lgkmcnt(3)
	v_mfma_f32_32x32x16_f16 v[114:129], v[134:137], v[170:173], v[114:129]
	v_mfma_f32_32x32x16_f16 v[34:49], v[134:137], v[174:177], v[34:49]
	ds_read_b128 v[134:137], v236 offset:4512
	s_waitcnt lgkmcnt(3)
	v_mfma_f32_32x32x16_f16 v[98:113], v[138:141], v[170:173], v[98:113]
	v_mfma_f32_32x32x16_f16 v[18:33], v[138:141], v[174:177], v[18:33]
	ds_read_b128 v[138:141], v236 offset:8864
	s_waitcnt lgkmcnt(3)
	v_mfma_f32_32x32x16_f16 v[66:81], v[142:145], v[170:173], v[66:81]
	v_mfma_f32_32x32x16_f16 v[2:17], v[142:145], v[174:177], v[2:17]
	ds_read_b128 v[142:145], v236 offset:13216
	global_load_dwordx4 v[170:173], v239, s[56:57]
	global_load_dwordx4 v[174:177], v239, s[56:57] offset:512
	s_add_u32 s56, s56, 0x4000
	s_addc_u32 s57, s57, 0
	s_waitcnt vmcnt(12)
	s_waitcnt lgkmcnt(3)
	v_mfma_f32_32x32x16_f16 v[82:97], v[130:133], v[178:181], v[82:97]
	v_mfma_f32_32x32x16_f16 v[50:65], v[130:133], v[182:185], v[50:65]
	ds_read_b128 v[130:133], v236 offset:192
	s_waitcnt lgkmcnt(3)
	v_mfma_f32_32x32x16_f16 v[114:129], v[134:137], v[178:181], v[114:129]
	v_mfma_f32_32x32x16_f16 v[34:49], v[134:137], v[182:185], v[34:49]
	ds_read_b128 v[134:137], v236 offset:4544
	s_waitcnt lgkmcnt(3)
	v_mfma_f32_32x32x16_f16 v[98:113], v[138:141], v[178:181], v[98:113]
	v_mfma_f32_32x32x16_f16 v[18:33], v[138:141], v[182:185], v[18:33]
	ds_read_b128 v[138:141], v236 offset:8896
	s_waitcnt lgkmcnt(3)
	v_mfma_f32_32x32x16_f16 v[66:81], v[142:145], v[178:181], v[66:81]
	v_mfma_f32_32x32x16_f16 v[2:17], v[142:145], v[182:185], v[2:17]
	ds_read_b128 v[142:145], v236 offset:13248
	global_load_dwordx4 v[178:181], v239, s[56:57]
	global_load_dwordx4 v[182:185], v239, s[56:57] offset:512
	s_add_u32 s56, s56, 0x4000
	s_addc_u32 s57, s57, 0
	s_waitcnt vmcnt(23)
	v_cvt_pk_f16_f32 v204, v204, v205
	v_cvt_pk_f16_f32 v205, v206, v207
	ds_write_b64 v237, v[204:205] offset:34816
	s_waitcnt vmcnt(22)
	v_cvt_pk_f16_f32 v208, v208, v209
	v_cvt_pk_f16_f32 v209, v210, v211
	ds_write_b64 v237, v[208:209] offset:39168
	s_waitcnt vmcnt(21)
	v_cvt_pk_f16_f32 v212, v212, v213
	v_cvt_pk_f16_f32 v213, v214, v215
	ds_write_b64 v237, v[212:213] offset:43520
	s_waitcnt vmcnt(20)
	v_cvt_pk_f16_f32 v216, v216, v217
	v_cvt_pk_f16_f32 v217, v218, v219
	ds_write_b64 v237, v[216:217] offset:47872
	s_waitcnt vmcnt(19)
	v_cvt_pk_f16_f32 v220, v220, v221
	v_cvt_pk_f16_f32 v221, v222, v223
	ds_write_b64 v237, v[220:221] offset:52224
	s_waitcnt vmcnt(18)
	v_cvt_pk_f16_f32 v224, v224, v225
	v_cvt_pk_f16_f32 v225, v226, v227
	ds_write_b64 v237, v[224:225] offset:56576
	s_waitcnt vmcnt(17)
	v_cvt_pk_f16_f32 v228, v228, v229
	v_cvt_pk_f16_f32 v229, v230, v231
	ds_write_b64 v237, v[228:229] offset:60928
	s_waitcnt vmcnt(16)
	v_cvt_pk_f16_f32 v232, v232, v233
	v_cvt_pk_f16_f32 v233, v234, v235
	ds_write_b64 v237, v[232:233] offset:65280
	s_waitcnt vmcnt(12)
	s_waitcnt lgkmcnt(11)
	v_mfma_f32_32x32x16_f16 v[82:97], v[130:133], v[186:189], v[82:97]
	v_mfma_f32_32x32x16_f16 v[50:65], v[130:133], v[190:193], v[50:65]
	ds_read_b128 v[130:133], v236 offset:224
	s_waitcnt lgkmcnt(11)
	v_mfma_f32_32x32x16_f16 v[114:129], v[134:137], v[186:189], v[114:129]
	v_mfma_f32_32x32x16_f16 v[34:49], v[134:137], v[190:193], v[34:49]
	ds_read_b128 v[134:137], v236 offset:4576
	s_waitcnt lgkmcnt(11)
	v_mfma_f32_32x32x16_f16 v[98:113], v[138:141], v[186:189], v[98:113]
	v_mfma_f32_32x32x16_f16 v[18:33], v[138:141], v[190:193], v[18:33]
	ds_read_b128 v[138:141], v236 offset:8928
	s_waitcnt lgkmcnt(11)
	v_mfma_f32_32x32x16_f16 v[66:81], v[142:145], v[186:189], v[66:81]
	v_mfma_f32_32x32x16_f16 v[2:17], v[142:145], v[190:193], v[2:17]
	ds_read_b128 v[142:145], v236 offset:13280
	global_load_dwordx4 v[186:189], v239, s[56:57]
	global_load_dwordx4 v[190:193], v239, s[56:57] offset:512
	s_add_u32 s56, s56, 0x4000
	s_addc_u32 s57, s57, 0
	s_waitcnt vmcnt(12)
	s_waitcnt lgkmcnt(3)
	v_mfma_f32_32x32x16_f16 v[82:97], v[130:133], v[194:197], v[82:97]
	v_mfma_f32_32x32x16_f16 v[50:65], v[130:133], v[198:201], v[50:65]
	s_waitcnt lgkmcnt(2)
	v_mfma_f32_32x32x16_f16 v[114:129], v[134:137], v[194:197], v[114:129]
	v_mfma_f32_32x32x16_f16 v[34:49], v[134:137], v[198:201], v[34:49]
	s_waitcnt lgkmcnt(1)
	v_mfma_f32_32x32x16_f16 v[98:113], v[138:141], v[194:197], v[98:113]
	v_mfma_f32_32x32x16_f16 v[18:33], v[138:141], v[198:201], v[18:33]
	s_waitcnt lgkmcnt(0)
	v_mfma_f32_32x32x16_f16 v[66:81], v[142:145], v[194:197], v[66:81]
	v_mfma_f32_32x32x16_f16 v[2:17], v[142:145], v[198:201], v[2:17]
	global_load_dwordx4 v[194:197], v239, s[56:57]
	global_load_dwordx4 v[198:201], v239, s[56:57] offset:512
	s_add_u32 s56, s56, 0x4000
	s_addc_u32 s57, s57, 0
	s_waitcnt lgkmcnt(0)
	s_barrier
	ds_read_b128 v[130:133], v236 offset:34816
	ds_read_b128 v[134:137], v236 offset:39168
	ds_read_b128 v[138:141], v236 offset:43520
	ds_read_b128 v[142:145], v236 offset:47872
	s_waitcnt vmcnt(12)
	s_waitcnt lgkmcnt(3)
	v_mfma_f32_32x32x16_f16 v[82:97], v[130:133], v[146:149], v[82:97]
	v_mfma_f32_32x32x16_f16 v[50:65], v[130:133], v[150:153], v[50:65]
	ds_read_b128 v[130:133], v236 offset:34848
	s_waitcnt lgkmcnt(3)
	v_mfma_f32_32x32x16_f16 v[114:129], v[134:137], v[146:149], v[114:129]
	v_mfma_f32_32x32x16_f16 v[34:49], v[134:137], v[150:153], v[34:49]
	ds_read_b128 v[134:137], v236 offset:39200
	s_waitcnt lgkmcnt(3)
	v_mfma_f32_32x32x16_f16 v[98:113], v[138:141], v[146:149], v[98:113]
	v_mfma_f32_32x32x16_f16 v[18:33], v[138:141], v[150:153], v[18:33]
	ds_read_b128 v[138:141], v236 offset:43552
	s_waitcnt lgkmcnt(3)
	v_mfma_f32_32x32x16_f16 v[66:81], v[142:145], v[146:149], v[66:81]
	v_mfma_f32_32x32x16_f16 v[2:17], v[142:145], v[150:153], v[2:17]
	ds_read_b128 v[142:145], v236 offset:47904
	global_load_dwordx4 v[146:149], v239, s[56:57]
	global_load_dwordx4 v[150:153], v239, s[56:57] offset:512
	s_add_u32 s56, s56, 0x4000
	s_addc_u32 s57, s57, 0
	s_waitcnt vmcnt(12)
	s_waitcnt lgkmcnt(3)
	v_mfma_f32_32x32x16_f16 v[82:97], v[130:133], v[154:157], v[82:97]
	v_mfma_f32_32x32x16_f16 v[50:65], v[130:133], v[158:161], v[50:65]
	ds_read_b128 v[130:133], v236 offset:34880
	s_waitcnt lgkmcnt(3)
	v_mfma_f32_32x32x16_f16 v[114:129], v[134:137], v[154:157], v[114:129]
	v_mfma_f32_32x32x16_f16 v[34:49], v[134:137], v[158:161], v[34:49]
	ds_read_b128 v[134:137], v236 offset:39232
	s_waitcnt lgkmcnt(3)
	v_mfma_f32_32x32x16_f16 v[98:113], v[138:141], v[154:157], v[98:113]
	v_mfma_f32_32x32x16_f16 v[18:33], v[138:141], v[158:161], v[18:33]
	ds_read_b128 v[138:141], v236 offset:43584
	s_waitcnt lgkmcnt(3)
	v_mfma_f32_32x32x16_f16 v[66:81], v[142:145], v[154:157], v[66:81]
	v_mfma_f32_32x32x16_f16 v[2:17], v[142:145], v[158:161], v[2:17]
	ds_read_b128 v[142:145], v236 offset:47936
	s_waitcnt vmcnt(10)
	s_waitcnt lgkmcnt(3)
	v_mfma_f32_32x32x16_f16 v[82:97], v[130:133], v[162:165], v[82:97]
	v_mfma_f32_32x32x16_f16 v[50:65], v[130:133], v[166:169], v[50:65]
	ds_read_b128 v[130:133], v236 offset:34912
	s_waitcnt lgkmcnt(3)
	v_mfma_f32_32x32x16_f16 v[114:129], v[134:137], v[162:165], v[114:129]
	v_mfma_f32_32x32x16_f16 v[34:49], v[134:137], v[166:169], v[34:49]
	ds_read_b128 v[134:137], v236 offset:39264
	s_waitcnt lgkmcnt(3)
	v_mfma_f32_32x32x16_f16 v[98:113], v[138:141], v[162:165], v[98:113]
	v_mfma_f32_32x32x16_f16 v[18:33], v[138:141], v[166:169], v[18:33]
	ds_read_b128 v[138:141], v236 offset:43616
	s_waitcnt lgkmcnt(3)
	v_mfma_f32_32x32x16_f16 v[66:81], v[142:145], v[162:165], v[66:81]
	v_mfma_f32_32x32x16_f16 v[2:17], v[142:145], v[166:169], v[2:17]
	ds_read_b128 v[142:145], v236 offset:47968
	s_waitcnt vmcnt(8)
	s_waitcnt lgkmcnt(3)
	v_mfma_f32_32x32x16_f16 v[82:97], v[130:133], v[170:173], v[82:97]
	v_mfma_f32_32x32x16_f16 v[50:65], v[130:133], v[174:177], v[50:65]
	ds_read_b128 v[130:133], v236 offset:34944
	s_waitcnt lgkmcnt(3)
	v_mfma_f32_32x32x16_f16 v[114:129], v[134:137], v[170:173], v[114:129]
	v_mfma_f32_32x32x16_f16 v[34:49], v[134:137], v[174:177], v[34:49]
	ds_read_b128 v[134:137], v236 offset:39296
	s_waitcnt lgkmcnt(3)
	v_mfma_f32_32x32x16_f16 v[98:113], v[138:141], v[170:173], v[98:113]
	v_mfma_f32_32x32x16_f16 v[18:33], v[138:141], v[174:177], v[18:33]
	ds_read_b128 v[138:141], v236 offset:43648
	s_waitcnt lgkmcnt(3)
	v_mfma_f32_32x32x16_f16 v[66:81], v[142:145], v[170:173], v[66:81]
	v_mfma_f32_32x32x16_f16 v[2:17], v[142:145], v[174:177], v[2:17]
	ds_read_b128 v[142:145], v236 offset:48000
	s_waitcnt vmcnt(6)
	s_waitcnt lgkmcnt(3)
	v_mfma_f32_32x32x16_f16 v[82:97], v[130:133], v[178:181], v[82:97]
	v_mfma_f32_32x32x16_f16 v[50:65], v[130:133], v[182:185], v[50:65]
	ds_read_b128 v[130:133], v236 offset:34976
	s_waitcnt lgkmcnt(3)
	v_mfma_f32_32x32x16_f16 v[114:129], v[134:137], v[178:181], v[114:129]
	v_mfma_f32_32x32x16_f16 v[34:49], v[134:137], v[182:185], v[34:49]
	ds_read_b128 v[134:137], v236 offset:39328
	s_waitcnt lgkmcnt(3)
	v_mfma_f32_32x32x16_f16 v[98:113], v[138:141], v[178:181], v[98:113]
	v_mfma_f32_32x32x16_f16 v[18:33], v[138:141], v[182:185], v[18:33]
	ds_read_b128 v[138:141], v236 offset:43680
	s_waitcnt lgkmcnt(3)
	v_mfma_f32_32x32x16_f16 v[66:81], v[142:145], v[178:181], v[66:81]
	v_mfma_f32_32x32x16_f16 v[2:17], v[142:145], v[182:185], v[2:17]
	ds_read_b128 v[142:145], v236 offset:48032
	s_waitcnt vmcnt(4)
	s_waitcnt lgkmcnt(3)
	v_mfma_f32_32x32x16_f16 v[82:97], v[130:133], v[186:189], v[82:97]
	v_mfma_f32_32x32x16_f16 v[50:65], v[130:133], v[190:193], v[50:65]
	ds_read_b128 v[130:133], v236 offset:35008
	s_waitcnt lgkmcnt(3)
	v_mfma_f32_32x32x16_f16 v[114:129], v[134:137], v[186:189], v[114:129]
	v_mfma_f32_32x32x16_f16 v[34:49], v[134:137], v[190:193], v[34:49]
	ds_read_b128 v[134:137], v236 offset:39360
	s_waitcnt lgkmcnt(3)
	v_mfma_f32_32x32x16_f16 v[98:113], v[138:141], v[186:189], v[98:113]
	v_mfma_f32_32x32x16_f16 v[18:33], v[138:141], v[190:193], v[18:33]
	ds_read_b128 v[138:141], v236 offset:43712
	s_waitcnt lgkmcnt(3)
	v_mfma_f32_32x32x16_f16 v[66:81], v[142:145], v[186:189], v[66:81]
	v_mfma_f32_32x32x16_f16 v[2:17], v[142:145], v[190:193], v[2:17]
	ds_read_b128 v[142:145], v236 offset:48064
	s_waitcnt vmcnt(2)
	s_waitcnt lgkmcnt(3)
	v_mfma_f32_32x32x16_f16 v[82:97], v[130:133], v[194:197], v[82:97]
	v_mfma_f32_32x32x16_f16 v[50:65], v[130:133], v[198:201], v[50:65]
	ds_read_b128 v[130:133], v236 offset:35040
	s_waitcnt lgkmcnt(3)
	v_mfma_f32_32x32x16_f16 v[114:129], v[134:137], v[194:197], v[114:129]
	v_mfma_f32_32x32x16_f16 v[34:49], v[134:137], v[198:201], v[34:49]
	ds_read_b128 v[134:137], v236 offset:39392
	s_waitcnt lgkmcnt(3)
	v_mfma_f32_32x32x16_f16 v[98:113], v[138:141], v[194:197], v[98:113]
	v_mfma_f32_32x32x16_f16 v[18:33], v[138:141], v[198:201], v[18:33]
	ds_read_b128 v[138:141], v236 offset:43744
	s_waitcnt lgkmcnt(3)
	v_mfma_f32_32x32x16_f16 v[66:81], v[142:145], v[194:197], v[66:81]
	v_mfma_f32_32x32x16_f16 v[2:17], v[142:145], v[198:201], v[2:17]
	ds_read_b128 v[142:145], v236 offset:48096
	s_waitcnt vmcnt(0)
	s_waitcnt lgkmcnt(3)
	v_mfma_f32_32x32x16_f16 v[82:97], v[130:133], v[146:149], v[82:97]
	v_mfma_f32_32x32x16_f16 v[50:65], v[130:133], v[150:153], v[50:65]
	s_waitcnt lgkmcnt(2)
	v_mfma_f32_32x32x16_f16 v[114:129], v[134:137], v[146:149], v[114:129]
	v_mfma_f32_32x32x16_f16 v[34:49], v[134:137], v[150:153], v[34:49]
	s_waitcnt lgkmcnt(1)
	v_mfma_f32_32x32x16_f16 v[98:113], v[138:141], v[146:149], v[98:113]
	v_mfma_f32_32x32x16_f16 v[18:33], v[138:141], v[150:153], v[18:33]
	s_waitcnt lgkmcnt(0)
	v_mfma_f32_32x32x16_f16 v[66:81], v[142:145], v[146:149], v[66:81]
	v_mfma_f32_32x32x16_f16 v[2:17], v[142:145], v[150:153], v[2:17]
	s_waitcnt vmcnt(0) lgkmcnt(0)
	s_nop 15
	s_mov_b64 exec, -1
	v_bfe_u32 v202, v0, 5, 1
	s_lshl_b32 s34, s29, 9
	v_and_b32_e32 v203, 0x1c0, v0
	v_and_b32_e32 v204, 31, v0
	v_or3_b32 v0, s34, v203, v204
	v_lshlrev_b32_e32 v0, 2, v0
	s_waitcnt vmcnt(0) lgkmcnt(0)
	s_barrier
	global_load_dword v131, v0, s[8:9]
	v_mov_b32_e32 v1, 0
	s_mov_b32 s6, 0x41a00000
	v_lshl_add_u64 v[0:1], s[8:9], 0, v[0:1]
	s_waitcnt vmcnt(0)
	v_cmp_nlt_f32_e32 vcc, s6, v131
	s_and_saveexec_b64 s[0:1], vcc
	s_cbranch_execz .LBB1_14
	v_mul_f32_e32 v130, 0x3fb8aa3b, v131
	s_mov_b32 s7, 0x3fb8aa3b
	v_rndne_f32_e32 v132, v130
	v_sub_f32_e32 v133, v130, v132
	v_fma_f32 v130, v131, s7, -v130
	v_fmamk_f32 v130, v131, 0x32a5705f, v130
	v_add_f32_e32 v130, v133, v130
	v_exp_f32_e32 v130, v130
	v_cvt_i32_f32_e32 v132, v132
	s_mov_b32 s7, 0xc2ce8ed0
	v_cmp_ngt_f32_e32 vcc, s7, v131
	s_mov_b32 s7, 0x42b17218
	v_ldexp_f32 v130, v130, v132
	v_cndmask_b32_e32 v130, 0, v130, vcc
	v_mov_b32_e32 v144, 0x7f800000
	v_cmp_nlt_f32_e32 vcc, s7, v131
	s_mov_b32 s7, 0x3f2aaaab
	s_mov_b32 s8, 0x7f800000
	v_cndmask_b32_e32 v145, v144, v130, vcc
	v_add_f32_e32 v132, 1.0, v145
	v_add_f32_e32 v130, -1.0, v132
	v_sub_f32_e32 v131, v130, v132
	v_add_f32_e32 v131, 1.0, v131
	v_sub_f32_e32 v130, v145, v130
	v_add_f32_e32 v133, v130, v131
	v_frexp_mant_f32_e32 v134, v132
	v_cvt_f64_f32_e32 v[130:131], v132
	v_frexp_exp_i32_f64_e32 v130, v[130:131]
	v_cmp_gt_f32_e32 vcc, s7, v134
	s_mov_b32 s7, 0x3f317218
	s_nop 0
	v_subbrev_co_u32_e32 v138, vcc, 0, v130, vcc
	v_sub_u32_e32 v130, 0, v138
	v_ldexp_f32 v131, v132, v130
	v_add_f32_e32 v132, -1.0, v131
	v_add_f32_e32 v134, 1.0, v131
	v_ldexp_f32 v130, v133, v130
	v_add_f32_e32 v133, 1.0, v132
	v_add_f32_e32 v135, -1.0, v134
	v_sub_f32_e32 v133, v131, v133
	v_sub_f32_e32 v131, v131, v135
	v_add_f32_e32 v133, v130, v133
	v_add_f32_e32 v130, v130, v131
	v_add_f32_e32 v139, v134, v130
	v_rcp_f32_e32 v141, v139
	v_sub_f32_e32 v131, v134, v139
	v_add_f32_e32 v140, v130, v131
	v_add_f32_e32 v131, v132, v133
	v_mul_f32_e32 v143, v131, v141
	v_sub_f32_e32 v130, v132, v131
	v_mul_f32_e32 v132, v139, v143
	v_fma_f32 v134, v143, v139, -v132
	v_fmac_f32_e32 v134, v143, v140
	v_add_f32_e32 v142, v133, v130
	v_add_f32_e32 v130, v132, v134
	v_sub_f32_e32 v133, v131, v130
	v_pk_add_f32 v[136:137], v[130:131], v[132:133] neg_lo:[0,1] neg_hi:[0,1]
	v_mov_b32_e32 v135, v130
	v_pk_add_f32 v[130:131], v[136:137], v[134:135] neg_lo:[0,1] neg_hi:[0,1]
	v_cmp_neq_f32_e32 vcc, s8, v145
	v_add_f32_e32 v131, v142, v131
	v_add_f32_e32 v130, v130, v131
	v_add_f32_e32 v131, v133, v130
	v_mul_f32_e32 v142, v141, v131
	v_mul_f32_e32 v132, v139, v142
	v_fma_f32 v134, v142, v139, -v132
	v_fmac_f32_e32 v134, v142, v140
	v_sub_f32_e32 v133, v133, v131
	v_add_f32_e32 v139, v130, v133
	v_add_f32_e32 v130, v132, v134
	v_sub_f32_e32 v133, v131, v130
	v_pk_add_f32 v[136:137], v[130:131], v[132:133] neg_lo:[0,1] neg_hi:[0,1]
	v_mov_b32_e32 v135, v130
	v_pk_add_f32 v[130:131], v[136:137], v[134:135] neg_lo:[0,1] neg_hi:[0,1]
	v_cvt_f32_i32_e32 v132, v138
	v_add_f32_e32 v131, v139, v131
	v_add_f32_e32 v130, v130, v131
	v_add_f32_e32 v130, v133, v130
	v_add_f32_e32 v133, v143, v142
	v_sub_f32_e32 v131, v133, v143
	v_mul_f32_e32 v130, v141, v130
	v_sub_f32_e32 v131, v142, v131
	v_add_f32_e32 v130, v131, v130
	v_add_f32_e32 v134, v133, v130
	v_mul_f32_e32 v136, v134, v134
	v_mov_b32_e32 v131, 0x3ecc95a3
	v_sub_f32_e32 v133, v134, v133
	v_fmac_f32_e32 v131, 0x3e9b6dac, v136
	v_sub_f32_e32 v130, v130, v133
	v_fmaak_f32 v131, v136, v131, 0x3f2aaada
	v_ldexp_f32 v137, v130, 1
	v_mul_f32_e32 v133, v134, v136
	v_mov_b32_e32 v130, 0x3f317218
	v_pk_mul_f32 v[130:131], v[132:133], v[130:131]
	v_ldexp_f32 v135, v134, 1
	v_fma_f32 v133, v132, s7, -v130
	v_fmamk_f32 v134, v132, 0xb102e308, v133
	v_pk_add_f32 v[132:133], v[130:131], v[134:135]
	v_mov_b32_e32 v136, v130
	v_sub_f32_e32 v135, v133, v135
	v_sub_f32_e32 v135, v131, v135
	v_add_f32_e32 v137, v137, v135
	v_pk_add_f32 v[130:131], v[132:133], v[130:131] neg_lo:[0,1] neg_hi:[0,1]
	v_pk_add_f32 v[138:139], v[132:133], v[136:137]
	v_mov_b32_e32 v135, v132
	v_mov_b32_e32 v131, v139
	v_pk_add_f32 v[140:141], v[134:135], v[130:131] neg_lo:[0,1] neg_hi:[0,1]
	v_pk_add_f32 v[130:131], v[134:135], v[130:131]
	v_mov_b32_e32 v136, v137
	v_pk_add_f32 v[134:135], v[130:131], v[132:133] op_sel:[1,0] op_sel_hi:[0,1] neg_lo:[0,1] neg_hi:[0,1]
	v_pk_add_f32 v[142:143], v[138:139], v[134:135] op_sel_hi:[1,0] neg_lo:[0,1] neg_hi:[0,1]
	v_mov_b32_e32 v138, v139
	v_mov_b32_e32 v139, v131
	v_pk_mov_b32 v[134:135], v[132:133], v[134:135] op_sel:[1,0]
	v_mov_b32_e32 v137, v132
	v_pk_add_f32 v[134:135], v[138:139], v[134:135] neg_lo:[0,1] neg_hi:[0,1]
	v_mov_b32_e32 v142, v140
	v_pk_add_f32 v[132:133], v[136:137], v[134:135] neg_lo:[0,1] neg_hi:[0,1]
	v_mov_b32_e32 v141, v131
	v_pk_add_f32 v[134:135], v[142:143], v[132:133]
	s_mov_b32 s7, 0x33800000
	v_pk_add_f32 v[136:137], v[134:135], v[134:135] op_sel:[0,1] op_sel_hi:[1,0]
	s_nop 0
	v_pk_add_f32 v[130:131], v[130:131], v[136:137] op_sel:[1,0] op_sel_hi:[0,1]
	v_mov_b32_e32 v135, v130
	v_pk_add_f32 v[138:139], v[134:135], v[140:141] neg_lo:[0,1] neg_hi:[0,1]
	v_mov_b32_e32 v133, v136
	v_sub_f32_e32 v131, v134, v138
	v_pk_add_f32 v[132:133], v[132:133], v[138:139] neg_lo:[0,1] neg_hi:[0,1]
	v_sub_f32_e32 v131, v140, v131
	v_add_f32_e32 v131, v132, v131
	v_add_f32_e32 v131, v131, v133
	v_add_f32_e32 v130, v130, v131
	v_cndmask_b32_e32 v130, v144, v130, vcc
	v_cmp_lt_f32_e64 vcc, |v145|, s7
	s_nop 1
	v_cndmask_b32_e32 v131, v130, v145, vcc

	.amdhsa_kernel _Z9fused_oscPKfS0_PK15HIP_vector_typeIjLj4EEPfPyPj
		.amdhsa_group_segment_fixed_size 0
		.amdhsa_private_segment_fixed_size 0
		.amdhsa_kernarg_size 48
		.amdhsa_user_sgpr_count 2
		.amdhsa_user_sgpr_dispatch_ptr 0
		.amdhsa_user_sgpr_queue_ptr 0
		.amdhsa_user_sgpr_kernarg_segment_ptr 1
		.amdhsa_user_sgpr_dispatch_id 0
		.amdhsa_user_sgpr_kernarg_preload_length 0
		.amdhsa_user_sgpr_kernarg_preload_offset 0
		.amdhsa_user_sgpr_private_segment_size 0
		.amdhsa_uses_dynamic_stack 0
		.amdhsa_enable_private_segment 0
		.amdhsa_system_sgpr_workgroup_id_x 1
		.amdhsa_system_sgpr_workgroup_id_y 0
		.amdhsa_system_sgpr_workgroup_id_z 0
		.amdhsa_system_sgpr_workgroup_info 0
		.amdhsa_system_vgpr_workitem_id 0
		.amdhsa_next_free_vgpr 248
		.amdhsa_next_free_sgpr 58
		.amdhsa_accum_offset 248
		.amdhsa_reserve_vcc 1
		.amdhsa_float_round_mode_32 0
		.amdhsa_float_round_mode_16_64 0
		.amdhsa_float_denorm_mode_32 3
		.amdhsa_float_denorm_mode_16_64 3
		.amdhsa_dx10_clamp 1
		.amdhsa_ieee_mode 1
		.amdhsa_fp16_overflow 0
		.amdhsa_tg_split 0
		.amdhsa_exception_fp_ieee_invalid_op 0
		.amdhsa_exception_fp_denorm_src 0
		.amdhsa_exception_fp_ieee_div_zero 0
		.amdhsa_exception_fp_ieee_overflow 0
		.amdhsa_exception_fp_ieee_underflow 0
		.amdhsa_exception_fp_ieee_inexact 0
		.amdhsa_exception_int_div_zero 0
	.end_amdhsa_kernel

amdhsa.kernels:
  - .agpr_count:     0
    .args:
      - .actual_access:  read_only
        .address_space:  global
        .offset:         0
        .size:           8
        .value_kind:     global_buffer
      - .actual_access:  write_only
        .address_space:  global
        .offset:         8
        .size:           8
        .value_kind:     global_buffer
      - .address_space:  global
        .offset:         16
        .size:           8
        .value_kind:     global_buffer
      - .address_space:  global
        .offset:         24
        .size:           8
        .value_kind:     global_buffer
    .group_segment_fixed_size: 0
    .kernarg_segment_align: 8
    .kernarg_segment_size: 32
    .language:       OpenCL C
    .language_version:
      - 2
      - 0
    .max_flat_workgroup_size: 256
    .name:           _Z9convert_wPKfP15HIP_vector_typeIjLj4EEPjPy
    .private_segment_fixed_size: 0
    .sgpr_count:     18
    .sgpr_spill_count: 0
    .symbol:         _Z9convert_wPKfP15HIP_vector_typeIjLj4EEPjPy.kd
    .uniform_work_group_size: 1
    .uses_dynamic_stack: false
    .vgpr_count:     20
    .vgpr_spill_count: 0
    .wavefront_size: 64
  - .agpr_count:     0
    .args:
      - .actual_access:  read_only
        .address_space:  global
        .offset:         0
        .size:           8
        .value_kind:     global_buffer
      - .actual_access:  read_only
        .address_space:  global
        .offset:         8
        .size:           8
        .value_kind:     global_buffer
      - .address_space:  global
        .offset:         16
        .size:           8
        .value_kind:     global_buffer
      - .actual_access:  write_only
        .address_space:  global
        .offset:         24
        .size:           8
        .value_kind:     global_buffer
      - .address_space:  global
        .offset:         32
        .size:           8
        .value_kind:     global_buffer
      - .address_space:  global
        .offset:         40
        .size:           8
        .value_kind:     global_buffer
    .group_segment_fixed_size: 0
    .kernarg_segment_align: 8
    .kernarg_segment_size: 48
    .language:       OpenCL C
    .language_version:
      - 2
      - 0
    .max_flat_workgroup_size: 512
    .name:           _Z9fused_oscPKfS0_PK15HIP_vector_typeIjLj4EEPfPyPj
    .private_segment_fixed_size: 0
    .sgpr_count:     64
    .sgpr_spill_count: 0
    .symbol:         _Z9fused_oscPKfS0_PK15HIP_vector_typeIjLj4EEPfPyPj.kd
    .uniform_work_group_size: 1
    .uses_dynamic_stack: false
    .vgpr_count:     248
    .vgpr_spill_count: 0
    .wavefront_size: 64
